# attention: waves 4-7 run a rotated tile loop (P.V of previous tile, then Q.K^T + softmax) with a 3-slot V LDS ring, so each SIMD pairs softmax VALU with the partner's MFMA phase
# baseline (speedup 1.0000x reference)
; #define LAS __attribute__((address_space(3)))
; __device__ __forceinline__ int opaque_tid() { int t = threadIdx.x; asm volatile("" : "+v"(t)); return t; }
; __device__ __forceinline__ int v_rd_base(int lane) { return ((lane & 3) << 3) | (((lane >> 2) & 3) << 6) | (((lane >> 4) & 1) << 5) | (((lane >> 5) & 1) << 8); }
; __device__ __forceinline__ int v_st256(int k, int c) { const int kk = (k & ~0xC) | ((k & 4) << 1) | ((k & 8) >> 1); return ((kk >> 3) * 8 + (c >> 5)) * 512 + ((kk & 7) * 32 + (c & 31)) * 2; }
; #define SLOAD_A(k0) do { const bf16_t* vp_ = Vh + (long)(k0) * LDK + toff; const bf16_t* kp_ = Kh + (long)(k0) * LDK + toff; \
;     sa0 = *(const bf16x8*)kp_; sa1 = *(const bf16x8*)(kp_ + 32L * LDK); sa2 = *(const bf16x8*)vp_; sa3 = *(const bf16x8*)(vp_ + 128); } while (0)
; #define SWRITE_A(b) do { LAS char* vb_ = V_lds + (b) * SHM_V2 + vst00; LAS char* kb_ = K_lds + (b) * SHM_K2 + kst0; \
;     *(LAS bf16x8*)(kb_) = sa0; *(LAS bf16x8*)(kb_ + 8192) = sa1; *(LAS bf16x8*)(vb_) = sa2; *(LAS bf16x8*)(vb_ + 2048) = sa3; } while (0)
; template <int LDQ, int LDK, int LDO>
; __device__ __forceinline__ void attn_body256(const bf16_t* __restrict__ Qb, const bf16_t* __restrict__ Kh, const bf16_t* __restrict__ Vh, float* __restrict__ Ob, int seq, LAS char* lds) {
;   const int tid = opaque_tid(), wid = tid >> 6, lane = tid & 63, r32 = lane & 31, hi = lane >> 5;
;   LAS char* V_lds = lds; LAS char* K_lds = lds + 2 * SHM_V2;
;   LAS float* wsl = (LAS float*)(lds + 2 * SHM_V2 + 2 * SHM_K2) + wid * 64; LAS float* li_l = wsl; LAS float* al_l = wsl + 32;
;   float m_reg = -1e30f, l_reg = 0; f32x16 o[8] = {}; bf16x8 qr[8];
;   const bf16_t* Qw = Qb + (long)(wid * QBLK + r32) * LDQ + hi * 8;
; #pragma unroll
;   for (int d0 = 0; d0 < 8; ++d0) qr[d0] = *(const bf16x8*)(Qw + d0 * 16);
;   const int sr = tid >> 4, sc = (tid & 15) * 8;
;   const int vst00 = v_st256(sr, sc), kst0 = KSWZ(sr, sc * 2);
;   const unsigned toff = (unsigned)(sr * LDK + sc);
;   const int vb0 = (int)(uintptr_t)V_lds + v_rd_base(lane);
;   bf16x8 sa0, sa1, sa2, sa3;
;     ...
;   f32x16 p0, p1; float mn, al; bf16x8 pa0, pa1, pa2, pa3; const int NT = seq / KVBLK;
;   SLOAD_A(0); asm volatile("s_waitcnt vmcnt(0)" ::: "memory"); SWRITE_A(0); SLOAD_B(0); asm volatile("s_waitcnt vmcnt(0)" ::: "memory"); SWRITE_B(0); __syncthreads();
.LBB0_933:
	s_lshl_b64 s[8:9], s[10:11], 1
	s_add_u32 s6, s4, s8
	s_addc_u32 s7, s5, s9
	v_mov_b32_e32 v226, v241
	s_movk_i32 s82, 0xffe0
	v_ashrrev_i32_e32 v17, 1, v241
	v_bfe_u32 v231, v241, 5, 1
	v_bfi_b32 v2, s82, v17, v241
	v_mov_b64_e32 v[4:5], s[6:7]
	s_movk_i32 s6, 0x3080
	v_mad_i64_i32 v[4:5], s[6:7], v2, s6, v[4:5]
	v_lshlrev_b32_e32 v212, 4, v231
	v_mov_b32_e32 v213, v3
	v_lshlrev_b32_e32 v19, 3, v241
	v_lshl_add_u64 v[4:5], v[4:5], 0, v[212:213]
	v_ashrrev_i32_e32 v18, 4, v241
	v_and_b32_e32 v2, 0x78, v19
	s_movk_i32 s6, 0x1840
	global_load_dwordx4 v[164:167], v[4:5], off
	global_load_dwordx4 v[168:171], v[4:5], off offset:32
	global_load_dwordx4 v[172:175], v[4:5], off offset:64
	global_load_dwordx4 v[176:179], v[4:5], off offset:96
	global_load_dwordx4 v[180:183], v[4:5], off offset:128
	global_load_dwordx4 v[184:187], v[4:5], off offset:160
	global_load_dwordx4 v[188:191], v[4:5], off offset:192
	global_load_dwordx4 v[192:195], v[4:5], off offset:224
	v_mad_u64_u32 v[4:5], s[6:7], v18, s6, v[2:3]
	s_add_u32 s10, s16, s8
	v_mov_b32_e32 v5, v3
	s_addc_u32 s11, s17, s9
	v_lshlrev_b64 v[12:13], 1, v[4:5]
	v_lshl_add_u64 v[4:5], s[10:11], 0, v[12:13]
	s_mov_b32 s6, 0x61000
	s_waitcnt vmcnt(10)
	v_add_co_u32_e32 v8, vcc, s6, v4
	v_lshl_add_u64 v[14:15], s[18:19], 0, v[12:13]
	s_nop 0
	v_addc_co_u32_e32 v9, vcc, 0, v5, vcc
	global_load_dwordx4 v[4:7], v[4:5], off
	s_nop 0
	global_load_dwordx4 v[8:11], v[8:9], off
	s_nop 0
	global_load_dwordx4 v[196:199], v[14:15], off
	global_load_dwordx4 v[200:203], v[14:15], off offset:256
	s_waitcnt vmcnt(0)
	v_lshl_add_u64 v[14:15], s[24:25], 0, v[12:13]
	global_load_dwordx4 v[204:207], v[14:15], off
	global_load_dwordx4 v[208:211], v[14:15], off offset:256
	v_and_b32_e32 v15, 0x3fffffc0, v241
	v_lshlrev_b32_e32 v20, 4, v241
	v_and_b32_e32 v214, 0xffffffe0, v17
	v_lshlrev_b32_e32 v17, 1, v18
	v_lshl_add_u32 v232, v15, 2, s64
	v_and_b32_e32 v15, 3, v18
	v_lshrrev_b32_e32 v22, 1, v18
	v_and_b32_e32 v23, 0x7ffff0, v18
	v_bfe_u32 v24, v19, 5, 2
	v_and_b32_e32 v26, 0x70, v20
	v_and_b32_e32 v17, 8, v17
	v_lshlrev_b32_e32 v2, 1, v2
	s_movk_i32 s7, 0x60
	v_lshlrev_b32_e32 v21, 1, v241
	v_lshlrev_b32_e32 v18, 8, v18
	v_and_b32_e32 v25, 0xc0, v20
	v_and_or_b32 v15, v22, 4, v15
	s_add_i32 s6, 0, 0x10000
	v_bitop3_b32 v215, v212, v20, s65 bitop3:0x78
	v_bitop3_b32 v235, v212, v26, s7 bitop3:0x36
	s_movk_i32 s7, 0x80
	v_or3_b32 v17, v23, v17, v24
	v_and_b32_e32 v20, 48, v2
	v_bitop3_b32 v2, v2, v241, s65 bitop3:0x78
	v_and_b32_e32 v213, 31, v241
	v_and_b32_e32 v21, 32, v21
	v_bitop3_b32 v236, v212, v26, s7 bitop3:0x36
	s_movk_i32 s7, 0xa0
	v_lshlrev_b32_e32 v15, 6, v15
	v_lshl_add_u32 v16, v17, 9, 0
	v_add3_u32 v240, s6, v2, v18
	s_movk_i32 s11, 0x118
	s_add_u32 s8, s78, s8
	v_and_b32_e32 v14, 63, v241
	v_bitop3_b32 v237, v212, v26, s7 bitop3:0x36
	s_movk_i32 s7, 0xc0
	v_lshl_add_u32 v239, v213, 8, s6
	v_add3_u32 v241, v16, v15, v20
	s_movk_i32 s6, 0xe0
	v_and_or_b32 v2, v19, s11, v21
	s_addc_u32 s9, s79, s9
	v_mov_b32_e32 v16, v3
	v_mov_b32_e32 v17, v3
	v_bitop3_b32 v233, v212, v26, 32 bitop3:0x36
	v_bitop3_b32 v234, v212, v26, 64 bitop3:0x36
	v_bitop3_b32 v238, v212, v26, s7 bitop3:0x36
	v_bitop3_b32 v242, v212, v26, s6 bitop3:0x36
	v_cmp_gt_u32_e64 s[6:7], 32, v14
	v_add3_u32 v244, v25, 0, v2
	v_lshl_add_u64 v[216:217], s[78:79], 0, v[12:13]
	v_lshl_add_u64 v[218:219], s[8:9], 0, v[12:13]
	v_mov_b32_e32 v2, v3
	v_mov_b32_e32 v12, v3
	v_mov_b32_e32 v13, v3
	s_waitcnt vmcnt(5)
	ds_write_b128 v240, v[4:7]
	s_waitcnt vmcnt(4)
	ds_write_b128 v240, v[8:11] offset:8192
	s_waitcnt vmcnt(3)
	ds_write_b128 v241, v[196:199]
	s_waitcnt vmcnt(2)
	ds_write_b128 v241, v[200:203] offset:2048
	s_waitcnt vmcnt(0)
	v_mov_b32_e32 v4, v3
	v_mov_b32_e32 v5, v3
	v_mov_b32_e32 v6, v3
	v_mov_b32_e32 v7, v3
	v_mov_b32_e32 v8, v3
	v_mov_b32_e32 v9, v3
	v_mov_b32_e32 v10, v3
	v_mov_b32_e32 v11, v3
	v_mov_b32_e32 v14, v3
	v_mov_b32_e32 v15, v3
	v_mov_b64_e32 v[130:131], v[16:17]
	v_mov_b64_e32 v[114:115], v[16:17]
	v_mov_b64_e32 v[98:99], v[16:17]
	v_mov_b64_e32 v[82:83], v[16:17]
	v_mov_b64_e32 v[66:67], v[16:17]
	v_mov_b64_e32 v[50:51], v[16:17]
	v_mov_b64_e32 v[34:35], v[16:17]
	v_mov_b64_e32 v[128:129], v[14:15]
	v_mov_b64_e32 v[126:127], v[12:13]
	v_mov_b64_e32 v[124:125], v[10:11]
	v_mov_b64_e32 v[122:123], v[8:9]
	v_mov_b64_e32 v[120:121], v[6:7]
	v_mov_b64_e32 v[118:119], v[4:5]
	v_mov_b64_e32 v[116:117], v[2:3]
	v_mov_b64_e32 v[112:113], v[14:15]
	v_mov_b64_e32 v[110:111], v[12:13]
	v_mov_b64_e32 v[108:109], v[10:11]
	v_mov_b64_e32 v[106:107], v[8:9]
	v_mov_b64_e32 v[104:105], v[6:7]
	v_mov_b64_e32 v[102:103], v[4:5]
	v_mov_b64_e32 v[100:101], v[2:3]
	v_mov_b64_e32 v[96:97], v[14:15]
	v_mov_b64_e32 v[94:95], v[12:13]
	v_mov_b64_e32 v[92:93], v[10:11]
	v_mov_b64_e32 v[90:91], v[8:9]
	v_mov_b64_e32 v[88:89], v[6:7]
	v_mov_b64_e32 v[86:87], v[4:5]
	v_mov_b64_e32 v[84:85], v[2:3]
	v_mov_b64_e32 v[80:81], v[14:15]
	v_mov_b64_e32 v[78:79], v[12:13]
	v_mov_b64_e32 v[76:77], v[10:11]
	v_mov_b64_e32 v[74:75], v[8:9]
	v_mov_b64_e32 v[72:73], v[6:7]
	v_mov_b64_e32 v[70:71], v[4:5]
	v_mov_b64_e32 v[68:69], v[2:3]
	v_mov_b64_e32 v[64:65], v[14:15]
	v_mov_b64_e32 v[62:63], v[12:13]
	v_mov_b64_e32 v[60:61], v[10:11]
	v_mov_b64_e32 v[58:59], v[8:9]
	v_mov_b64_e32 v[56:57], v[6:7]
	v_mov_b64_e32 v[54:55], v[4:5]
	v_mov_b64_e32 v[52:53], v[2:3]
	v_mov_b64_e32 v[48:49], v[14:15]
	v_mov_b64_e32 v[46:47], v[12:13]
	v_mov_b64_e32 v[44:45], v[10:11]
	v_mov_b64_e32 v[42:43], v[8:9]
	v_mov_b64_e32 v[40:41], v[6:7]
	v_mov_b64_e32 v[38:39], v[4:5]
	v_mov_b64_e32 v[36:37], v[2:3]
	v_mov_b64_e32 v[32:33], v[14:15]
	v_mov_b64_e32 v[30:31], v[12:13]
	v_mov_b64_e32 v[28:29], v[10:11]
	v_mov_b64_e32 v[26:27], v[8:9]
	v_mov_b64_e32 v[24:25], v[6:7]
	v_mov_b64_e32 v[22:23], v[4:5]
	v_mov_b64_e32 v[20:21], v[2:3]
	v_mov_b64_e32 v[18:19], v[16:17]
	s_mov_b32 s10, 0
	v_lshl_add_u32 v243, v213, 2, v232
	v_mov_b32_e32 v245, 0
	v_mov_b32_e32 v248, 0xf149f2ca
	s_mov_b64 s[82:83], 0
	s_mov_b32 s86, 0x8000
	v_mov_b64_e32 v[16:17], v[14:15]
	v_mov_b64_e32 v[14:15], v[12:13]
	v_mov_b64_e32 v[12:13], v[10:11]
	v_mov_b64_e32 v[10:11], v[8:9]
	v_mov_b64_e32 v[8:9], v[6:7]
	v_mov_b64_e32 v[6:7], v[4:5]
	v_mov_b64_e32 v[4:5], v[2:3]
	s_waitcnt vmcnt(1)
	ds_write_b128 v241, v[204:207] offset:16384
	s_waitcnt vmcnt(0)
	ds_write_b128 v241, v[208:211] offset:18432
	s_waitcnt lgkmcnt(0)
	s_barrier
	s_mov_b32 s98, 0
	s_mov_b32 s99, 0x8000
	s_mov_b32 s100, 0x19000
	v_readfirstlane_b32 s101, v226
	s_nop 3
	s_lshr_b32 s101, s101, 8
	s_cmp_lg_u32 s101, 0
	s_cbranch_scc1 .Lattn_b_top

; #define LAS __attribute__((address_space(3)))
; #define SBAR() __builtin_amdgcn_sched_barrier(0)
; #define SLOAD_A(k0) do { const bf16_t* vp_ = Vh + (long)(k0) * LDK + toff; const bf16_t* kp_ = Kh + (long)(k0) * LDK + toff; \
;     sa0 = *(const bf16x8*)kp_; sa1 = *(const bf16x8*)(kp_ + 32L * LDK); sa2 = *(const bf16x8*)vp_; sa3 = *(const bf16x8*)(vp_ + 128); } while (0)
; __device__ __forceinline__ void qkt(f32x16& p0, f32x16& p1, const LAS char* Ks, const bf16x8* qr, int r32, int hi) {
;   p0 = f32x16{}; p1 = f32x16{};
; #pragma unroll
;   for (int d0 = 0; d0 < 8; ++d0) { int cb = (d0 * 16 + hi * 8) * 2;
;     bf16x8 b0 = *(const LAS bf16x8*)(Ks + KSWZ(r32, cb));
;     bf16x8 b1 = *(const LAS bf16x8*)(Ks + KSWZ(32 + r32, cb));
;     p0 = __builtin_amdgcn_mfma_f32_32x32x16_bf16(b0, qr[d0], p0, 0, 0, 0);
;     p1 = __builtin_amdgcn_mfma_f32_32x32x16_bf16(b1, qr[d0], p1, 0, 0, 0); }
; }
; template <int LDQ, int LDK, int LDO>
; __device__ __forceinline__ void attn_body256(const bf16_t* __restrict__ Qb, const bf16_t* __restrict__ Kh, const bf16_t* __restrict__ Vh, float* __restrict__ Ob, int seq, LAS char* lds) {
;     ...
;   for (int j = 0; j < NT; ++j) {
;     if (j + 1 < NT) SLOAD_A((j + 1) * KVBLK);
;     SBAR(); qkt(p0, p1, K_lds + (j & 1) * SHM_K2, qr, r32, hi);
.LBB0_936:
	s_add_i32 s87, s10, 1
	s_and_b32 s88, s10, 1
	v_lshl_add_u32 v2, s88, 14, v239
	v_add_u32_e32 v136, v2, v215
	ds_read_b128 v[132:135], v136
	ds_read_b128 v[136:139], v136 offset:8192
	v_add_u32_e32 v222, v2, v233
	ds_read_b128 v[250:253], v222
	ds_read_b128 v[222:225], v222 offset:8192
	v_add_u32_e32 v246, v2, v234
	s_waitcnt lgkmcnt(3)
	v_mfma_f32_32x32x16_bf16 v[148:163], v[132:135], v[164:167], 0
	s_mov_b32 s8, 0x42b504f3
	s_waitcnt lgkmcnt(2)
	v_mfma_f32_32x32x16_bf16 v[132:147], v[136:139], v[164:167], 0
	s_waitcnt lgkmcnt(1)
	v_mfma_f32_32x32x16_bf16 v[148:163], v[250:253], v[168:171], v[148:163]
	s_waitcnt lgkmcnt(0)
	v_mfma_f32_32x32x16_bf16 v[132:147], v[222:225], v[168:171], v[132:147]
	ds_read_b128 v[222:225], v246
	ds_read_b128 v[250:253], v246 offset:8192
	v_add_u32_e32 v246, v2, v235
	s_waitcnt lgkmcnt(1)
	v_mfma_f32_32x32x16_bf16 v[148:163], v[222:225], v[172:175], v[148:163]
	s_waitcnt lgkmcnt(0)
	v_mfma_f32_32x32x16_bf16 v[132:147], v[250:253], v[172:175], v[132:147]
	ds_read_b128 v[222:225], v246
	ds_read_b128 v[250:253], v246 offset:8192
	v_add_u32_e32 v246, v2, v236
	s_waitcnt lgkmcnt(1)
	v_mfma_f32_32x32x16_bf16 v[148:163], v[222:225], v[176:179], v[148:163]
	s_waitcnt lgkmcnt(0)
	v_mfma_f32_32x32x16_bf16 v[132:147], v[250:253], v[176:179], v[132:147]
	ds_read_b128 v[222:225], v246
	ds_read_b128 v[250:253], v246 offset:8192
	v_add_u32_e32 v246, v2, v237
	s_waitcnt lgkmcnt(1)
	v_mfma_f32_32x32x16_bf16 v[148:163], v[222:225], v[180:183], v[148:163]
	s_waitcnt lgkmcnt(0)
	v_mfma_f32_32x32x16_bf16 v[132:147], v[250:253], v[180:183], v[132:147]
	ds_read_b128 v[222:225], v246
	ds_read_b128 v[250:253], v246 offset:8192
	v_add_u32_e32 v246, v2, v238
	v_add_u32_e32 v2, v2, v242
	s_waitcnt lgkmcnt(1)
	v_mfma_f32_32x32x16_bf16 v[148:163], v[222:225], v[184:187], v[148:163]
	s_waitcnt lgkmcnt(0)
	v_mfma_f32_32x32x16_bf16 v[132:147], v[250:253], v[184:187], v[132:147]
	ds_read_b128 v[222:225], v246
	ds_read_b128 v[250:253], v246 offset:8192
	s_waitcnt lgkmcnt(1)
	v_mfma_f32_32x32x16_bf16 v[148:163], v[222:225], v[188:191], v[148:163]
	s_waitcnt lgkmcnt(0)
	v_mfma_f32_32x32x16_bf16 v[132:147], v[250:253], v[188:191], v[132:147]
	ds_read_b128 v[222:225], v2
	ds_read_b128 v[250:253], v2 offset:8192
	s_waitcnt lgkmcnt(1)
	v_mfma_f32_32x32x16_bf16 v[148:163], v[222:225], v[192:195], v[148:163]
	s_waitcnt lgkmcnt(0)
; #define SWRITE_A(b) do { LAS char* vb_ = V_lds + (b) * SHM_V2 + vst00; LAS char* kb_ = K_lds + (b) * SHM_K2 + kst0; \
;     *(LAS bf16x8*)(kb_) = sa0; *(LAS bf16x8*)(kb_ + 8192) = sa1; *(LAS bf16x8*)(vb_) = sa2; *(LAS bf16x8*)(vb_ + 2048) = sa3; } while (0)
; #define SLOAD_B(k0) do { const bf16_t* vp_ = Vh + (long)((k0) + 32) * LDK + toff; sa0 = *(const bf16x8*)vp_; sa1 = *(const bf16x8*)(vp_ + 128); } while (0)
; __device__ __forceinline__ void partialSM(f32x16& p0, f32x16& p1, float& m_reg, float& mn, float& alpha) {
;   constexpr float C = SCALE * 1.4426950408889634f;
;   float pmax = p0[0]; for (int r = 1; r < 16; ++r) pmax = fmaxf(pmax, p0[r]); for (int r = 0; r < 16; ++r) pmax = fmaxf(pmax, p1[r]);
;   { auto rr = __builtin_amdgcn_permlane32_swap(__float_as_uint(pmax), __float_as_uint(pmax), false, false);
;     pmax = fmaxf(__uint_as_float(rr[0]), __uint_as_float(rr[1])); }
;   if (__builtin_expect(__all(pmax - m_reg <= THR / SCALE), 1)) { mn = m_reg; alpha = 1.f; }
;   else { mn = fmaxf(m_reg, pmax); alpha = __builtin_amdgcn_exp2f((m_reg - mn) * C); m_reg = mn; }
;   float mnC = -mn * C;
;   for (int r = 0; r < 16; ++r) p0[r] = fmaf(p0[r], C, mnC); for (int r = 0; r < 16; ++r) p1[r] = fmaf(p1[r], C, mnC);
;   for (int r = 0; r < 16; ++r) p0[r] = __builtin_amdgcn_exp2f(p0[r]);
; }
; __device__ __forceinline__ void finishSM(f32x16& p0, f32x16& p1, float alpha, float& l_reg, bf16x8& pa0, bf16x8& pa1, bf16x8& pa2, bf16x8& pa3) {
;   for (int r = 0; r < 16; ++r) p1[r] = __builtin_amdgcn_exp2f(p1[r]);
;   float ps = 0; for (int r = 0; r < 16; ++r) ps += p0[r]; for (int r = 0; r < 16; ++r) ps += p1[r];
;   { auto rr = __builtin_amdgcn_permlane32_swap(__float_as_uint(ps), __float_as_uint(ps), false, false);
;     ps = __uint_as_float(rr[0]) + __uint_as_float(rr[1]); }
;   l_reg = l_reg * alpha + ps;
;     ...
;   PK4(p0, 0, pa0); PK4(p0, 8, pa1); PK4(p1, 0, pa2); PK4(p1, 8, pa3);
; template <int LDQ, int LDK, int LDO>
; __device__ __forceinline__ void attn_body256(const bf16_t* __restrict__ Qb, const bf16_t* __restrict__ Kh, const bf16_t* __restrict__ Vh, float* __restrict__ Ob, int seq, LAS char* lds) {
;     ...
;     if (j + 1 < NT) { asm volatile("s_waitcnt vmcnt(0)" ::: "memory"); SWRITE_A((j + 1) & 1); SLOAD_B((j + 1) * KVBLK); }
	v_mfma_f32_32x32x16_bf16 v[132:147], v[250:253], v[192:195], v[132:147]
	s_nop 9
	v_max_f32_e32 v2, v149, v149
	v_max_f32_e32 v222, v148, v148
	v_max_f32_e32 v2, v222, v2
	v_max3_f32 v2, v2, v150, v151
	v_max3_f32 v2, v2, v152, v153
	v_max3_f32 v2, v2, v154, v155
	v_max3_f32 v2, v2, v156, v157
	v_max3_f32 v2, v2, v158, v159
	v_max3_f32 v2, v2, v160, v161
	v_max3_f32 v2, v2, v162, v163
	v_max3_f32 v2, v2, v132, v133
	v_max3_f32 v2, v2, v134, v135
	v_max3_f32 v2, v2, v136, v137
	v_max3_f32 v2, v2, v138, v139
	v_max3_f32 v2, v2, v140, v141
	v_max3_f32 v2, v2, v142, v143
	v_max3_f32 v2, v2, v144, v145
	v_max3_f32 v2, v2, v146, v147
	v_mov_b32_e32 v222, v2
	s_nop 1
	v_permlane32_swap_b32_e32 v2, v222
	v_max_f32_e32 v222, v222, v222
	v_max_f32_e32 v2, v2, v2
	v_max_f32_e32 v2, v2, v222
	v_sub_f32_e32 v222, v2, v248
	v_cmp_ge_f32_e32 vcc, s8, v222
	s_cmp_eq_u64 vcc, exec
	v_max_f32_e32 v222, v248, v248
	s_cselect_b64 s[10:11], -1, 0
	v_max_f32_e32 v249, v222, v2
	v_cndmask_b32_e64 v2, v249, v248, s[10:11]
	v_mul_f32_e32 v222, 0xbe0293ee, v2
	v_fmamk_f32 v148, v148, 0x3e0293ee, v222
	v_fmamk_f32 v149, v149, 0x3e0293ee, v222
	v_fmamk_f32 v150, v150, 0x3e0293ee, v222
	v_fmamk_f32 v151, v151, 0x3e0293ee, v222
	v_fmamk_f32 v152, v152, 0x3e0293ee, v222
	v_fmamk_f32 v153, v153, 0x3e0293ee, v222
	v_fmamk_f32 v154, v154, 0x3e0293ee, v222
	v_fmamk_f32 v155, v155, 0x3e0293ee, v222
	v_fmamk_f32 v156, v156, 0x3e0293ee, v222
	v_fmamk_f32 v157, v157, 0x3e0293ee, v222
	v_fmamk_f32 v158, v158, 0x3e0293ee, v222
	v_fmamk_f32 v159, v159, 0x3e0293ee, v222
	v_fmamk_f32 v160, v160, 0x3e0293ee, v222
	v_fmamk_f32 v161, v161, 0x3e0293ee, v222
	v_fmamk_f32 v162, v162, 0x3e0293ee, v222
	v_fmamk_f32 v163, v163, 0x3e0293ee, v222
	v_fmamk_f32 v132, v132, 0x3e0293ee, v222
	v_fmamk_f32 v133, v133, 0x3e0293ee, v222
	v_fmamk_f32 v134, v134, 0x3e0293ee, v222
	v_fmamk_f32 v135, v135, 0x3e0293ee, v222
	v_fmamk_f32 v136, v136, 0x3e0293ee, v222
	v_fmamk_f32 v137, v137, 0x3e0293ee, v222
	v_fmamk_f32 v138, v138, 0x3e0293ee, v222
	v_fmamk_f32 v139, v139, 0x3e0293ee, v222
	v_fmamk_f32 v140, v140, 0x3e0293ee, v222
	v_fmamk_f32 v141, v141, 0x3e0293ee, v222
	v_fmamk_f32 v142, v142, 0x3e0293ee, v222
	v_fmamk_f32 v143, v143, 0x3e0293ee, v222
	v_fmamk_f32 v144, v144, 0x3e0293ee, v222
	v_fmamk_f32 v145, v145, 0x3e0293ee, v222
	v_fmamk_f32 v146, v146, 0x3e0293ee, v222
	v_fmac_f32_e32 v222, 0x3e0293ee, v147
	v_exp_f32_e32 v147, v148
	v_exp_f32_e32 v148, v149
	v_exp_f32_e32 v149, v150
	v_exp_f32_e32 v150, v151
	v_exp_f32_e32 v151, v152
	v_exp_f32_e32 v152, v153
	v_exp_f32_e32 v153, v154
	v_exp_f32_e32 v154, v155
	v_exp_f32_e32 v155, v156
	v_exp_f32_e32 v156, v157
	v_exp_f32_e32 v157, v158
	v_exp_f32_e32 v158, v159
	v_exp_f32_e32 v159, v160
	v_exp_f32_e32 v160, v161
	v_exp_f32_e32 v161, v162
	v_exp_f32_e32 v162, v163
	v_exp_f32_e32 v163, v132
	v_add_f32_e32 v132, 0, v147
	v_add_f32_e32 v132, v148, v132
	v_add_f32_e32 v132, v149, v132
	v_add_f32_e32 v132, v150, v132
	v_add_f32_e32 v132, v151, v132
	v_add_f32_e32 v132, v152, v132
	v_add_f32_e32 v132, v153, v132
	v_add_f32_e32 v132, v154, v132
	v_add_f32_e32 v132, v155, v132
	v_add_f32_e32 v132, v156, v132
	v_add_f32_e32 v132, v157, v132
	v_add_f32_e32 v132, v158, v132
	v_add_f32_e32 v132, v159, v132
	v_exp_f32_e32 v223, v133
	v_add_f32_e32 v132, v160, v132
	v_exp_f32_e32 v224, v134
	v_add_f32_e32 v132, v161, v132
	v_exp_f32_e32 v225, v135
	v_add_f32_e32 v132, v162, v132
	v_exp_f32_e32 v250, v136
	v_add_f32_e32 v132, v163, v132
	v_exp_f32_e32 v251, v137
	v_add_f32_e32 v132, v223, v132
	v_exp_f32_e32 v252, v138
	v_add_f32_e32 v132, v224, v132
	v_exp_f32_e32 v253, v139
	v_add_f32_e32 v132, v225, v132
	v_exp_f32_e32 v254, v140
	v_add_f32_e32 v132, v250, v132
	v_exp_f32_e32 v0, v141
	v_add_f32_e32 v132, v251, v132
	v_exp_f32_e32 v1, v142
	v_add_f32_e32 v132, v252, v132
	v_exp_f32_e32 v227, v143
	v_add_f32_e32 v132, v253, v132
	v_exp_f32_e32 v228, v144
	v_add_f32_e32 v132, v254, v132
	v_exp_f32_e32 v229, v145
	v_add_f32_e32 v132, v0, v132
	v_exp_f32_e32 v230, v146
	v_add_f32_e32 v132, v1, v132
	v_exp_f32_e32 v222, v222
	v_add_f32_e32 v132, v227, v132
	v_add_f32_e32 v132, v228, v132
	v_add_f32_e32 v132, v229, v132
	v_add_f32_e32 v132, v230, v132
	v_add_f32_e32 v246, v222, v132
	v_mov_b32_e32 v247, v246
	v_cvt_pk_bf16_f32 v132, v147, v148
	v_cvt_pk_bf16_f32 v133, v149, v150
	v_cvt_pk_bf16_f32 v134, v151, v152
	v_cvt_pk_bf16_f32 v135, v153, v154
	v_cvt_pk_bf16_f32 v136, v155, v156
	v_cvt_pk_bf16_f32 v137, v157, v158
	v_cvt_pk_bf16_f32 v138, v159, v160
	v_cvt_pk_bf16_f32 v139, v161, v162
	v_cvt_pk_bf16_f32 v140, v163, v223
	v_cvt_pk_bf16_f32 v141, v224, v225
	v_cvt_pk_bf16_f32 v142, v250, v251
	v_cvt_pk_bf16_f32 v143, v252, v253
	v_cvt_pk_bf16_f32 v144, v254, v0
	v_cvt_pk_bf16_f32 v145, v1, v227
	v_cvt_pk_bf16_f32 v146, v228, v229
	v_cvt_pk_bf16_f32 v147, v230, v222
	s_nop 1
	v_permlane32_swap_b32_e32 v246, v247
	v_permlane32_swap_b32_e32 v132, v134
	v_permlane32_swap_b32_e32 v133, v135
	v_permlane32_swap_b32_e32 v136, v138
	v_permlane32_swap_b32_e32 v137, v139
	v_permlane32_swap_b32_e32 v140, v142
	v_permlane32_swap_b32_e32 v141, v143
	v_permlane32_swap_b32_e32 v144, v146
	v_permlane32_swap_b32_e32 v145, v147
	v_cndmask_b32_e64 v0, 0, 1, s[84:85]
	v_cmp_ne_u32_e64 s[8:9], 1, v0
	s_andn2_b64 vcc, exec, s[84:85]
	s_cbranch_vccnz .LBB0_938
	s_and_b32 s84, s87, 1
	v_lshl_add_u32 v1, s84, 14, v240
	v_add_co_u32_e32 v148, vcc, 0x125000, v220
	s_waitcnt vmcnt(0)
	v_add_u32_e32 v0, s99, v241
	s_waitcnt vmcnt(1)
	ds_write_b128 v1, v[204:207]
	s_waitcnt vmcnt(0)
	ds_write_b128 v1, v[208:211] offset:8192
	s_waitcnt vmcnt(1)
	ds_write_b128 v0, v[196:199]
	s_waitcnt vmcnt(0)
	ds_write_b128 v0, v[200:203] offset:2048
	v_addc_co_u32_e32 v149, vcc, 0, v221, vcc
	global_load_dwordx4 v[204:207], v[148:149], off
	global_load_dwordx4 v[208:211], v[148:149], off offset:256

; #define SBAR() __builtin_amdgcn_sched_barrier(0)
; #define SWRITE_B(b) do { LAS char* vb_ = V_lds + (b) * SHM_V2 + vst00; *(LAS bf16x8*)(vb_ + 16384) = sa0; *(LAS bf16x8*)(vb_ + 18432) = sa1; } while (0)
; template <int D0> __device__ __forceinline__ void pv_one256(f32x16& od, int vb, bf16x8 pa0, bf16x8 pa1, bf16x8 pa2, bf16x8 pa3) {
;   const s16x4 l0 = tr_read<v_rd_off256(D0, 0, 0)>(vb), h0 = tr_read<v_rd_off256(D0, 0, 1)>(vb), l1 = tr_read<v_rd_off256(D0, 1, 0)>(vb), h1 = tr_read<v_rd_off256(D0, 1, 1)>(vb);
;   const s16x4 l2 = tr_read<v_rd_off256(D0, 2, 0)>(vb), h2 = tr_read<v_rd_off256(D0, 2, 1)>(vb), l3 = tr_read<v_rd_off256(D0, 3, 0)>(vb), h3 = tr_read<v_rd_off256(D0, 3, 1)>(vb);
;   asm volatile("s_waitcnt lgkmcnt(0)" ::: "memory"); SBAR();
;     ...
;   od = __builtin_amdgcn_mfma_f32_32x32x16_bf16(pa0, PK(l0, h0), od, 0, 0, 0);
;   od = __builtin_amdgcn_mfma_f32_32x32x16_bf16(pa1, PK(l1, h1), od, 0, 0, 0);
;   od = __builtin_amdgcn_mfma_f32_32x32x16_bf16(pa2, PK(l2, h2), od, 0, 0, 0);
;   od = __builtin_amdgcn_mfma_f32_32x32x16_bf16(pa3, PK(l3, h3), od, 0, 0, 0);
;     ...
; }
; template <int LDQ, int LDK, int LDO>
; __device__ __forceinline__ void attn_body256(const bf16_t* __restrict__ Qb, const bf16_t* __restrict__ Kh, const bf16_t* __restrict__ Vh, float* __restrict__ Ob, int seq, LAS char* lds) {
;     ...
;     { const int vb = vb0 + (j & 1) * SHM_V2;
;       pv_one256<0>(o[0], vb, pa0, pa1, pa2, pa3); pv_one256<1>(o[1], vb, pa0, pa1, pa2, pa3); pv_one256<2>(o[2], vb, pa0, pa1, pa2, pa3); pv_one256<3>(o[3], vb, pa0, pa1, pa2, pa3);
;       pv_one256<4>(o[4], vb, pa0, pa1, pa2, pa3); pv_one256<5>(o[5], vb, pa0, pa1, pa2, pa3); pv_one256<6>(o[6], vb, pa0, pa1, pa2, pa3); pv_one256<7>(o[7], vb, pa0, pa1, pa2, pa3); }
;     if (j + 1 < NT) { asm volatile("s_waitcnt vmcnt(0)" ::: "memory"); SWRITE_B((j + 1) & 1); }
.LBB0_942:
	v_add_u32_e32 v0, s98, v244
	ds_read_b64_tr_b16 v[148:149], v0 offset:0
	ds_read_b64_tr_b16 v[150:151], v0 offset:0x1000
	ds_read_b64_tr_b16 v[152:153], v0 offset:0x2000
	ds_read_b64_tr_b16 v[154:155], v0 offset:0x3000
	ds_read_b64_tr_b16 v[156:157], v0 offset:0x4000
	ds_read_b64_tr_b16 v[158:159], v0 offset:0x5000
	ds_read_b64_tr_b16 v[160:161], v0 offset:0x6000
	ds_read_b64_tr_b16 v[162:163], v0 offset:0x7000
	s_waitcnt lgkmcnt(0)
	s_nop 0
	v_mfma_f32_32x32x16_bf16 v[116:131], v[132:135], v[148:151], v[116:131]
	ds_read_b64_tr_b16 v[148:149], v0 offset:0x200
	ds_read_b64_tr_b16 v[150:151], v0 offset:0x1200
	v_mfma_f32_32x32x16_bf16 v[116:131], v[136:139], v[152:155], v[116:131]
	ds_read_b64_tr_b16 v[152:153], v0 offset:0x2200
	ds_read_b64_tr_b16 v[154:155], v0 offset:0x3200
	v_mfma_f32_32x32x16_bf16 v[116:131], v[140:143], v[156:159], v[116:131]
	ds_read_b64_tr_b16 v[156:157], v0 offset:0x4200
	ds_read_b64_tr_b16 v[158:159], v0 offset:0x5200
	v_mfma_f32_32x32x16_bf16 v[116:131], v[144:147], v[160:163], v[116:131]
	ds_read_b64_tr_b16 v[160:161], v0 offset:0x6200
	ds_read_b64_tr_b16 v[162:163], v0 offset:0x7200
	s_waitcnt lgkmcnt(0)
	v_mfma_f32_32x32x16_bf16 v[100:115], v[132:135], v[148:151], v[100:115]
	ds_read_b64_tr_b16 v[148:149], v0 offset:0x400
	ds_read_b64_tr_b16 v[150:151], v0 offset:0x1400
	v_mfma_f32_32x32x16_bf16 v[100:115], v[136:139], v[152:155], v[100:115]
	ds_read_b64_tr_b16 v[152:153], v0 offset:0x2400
	ds_read_b64_tr_b16 v[154:155], v0 offset:0x3400
	v_mfma_f32_32x32x16_bf16 v[100:115], v[140:143], v[156:159], v[100:115]
	ds_read_b64_tr_b16 v[156:157], v0 offset:0x4400
	ds_read_b64_tr_b16 v[158:159], v0 offset:0x5400
	v_mfma_f32_32x32x16_bf16 v[100:115], v[144:147], v[160:163], v[100:115]
	ds_read_b64_tr_b16 v[160:161], v0 offset:0x6400
	ds_read_b64_tr_b16 v[162:163], v0 offset:0x7400
	s_waitcnt lgkmcnt(0)
	v_mfma_f32_32x32x16_bf16 v[84:99], v[132:135], v[148:151], v[84:99]
	ds_read_b64_tr_b16 v[148:149], v0 offset:0x600
	ds_read_b64_tr_b16 v[150:151], v0 offset:0x1600
	v_mfma_f32_32x32x16_bf16 v[84:99], v[136:139], v[152:155], v[84:99]
	ds_read_b64_tr_b16 v[152:153], v0 offset:0x2600
	ds_read_b64_tr_b16 v[154:155], v0 offset:0x3600
	v_mfma_f32_32x32x16_bf16 v[84:99], v[140:143], v[156:159], v[84:99]
	ds_read_b64_tr_b16 v[156:157], v0 offset:0x4600
	ds_read_b64_tr_b16 v[158:159], v0 offset:0x5600
	v_mfma_f32_32x32x16_bf16 v[84:99], v[144:147], v[160:163], v[84:99]
	ds_read_b64_tr_b16 v[160:161], v0 offset:0x6600
	ds_read_b64_tr_b16 v[162:163], v0 offset:0x7600
	s_waitcnt lgkmcnt(0)
	v_mfma_f32_32x32x16_bf16 v[68:83], v[132:135], v[148:151], v[68:83]
	ds_read_b64_tr_b16 v[148:149], v0 offset:0x800
	ds_read_b64_tr_b16 v[150:151], v0 offset:0x1800
	v_mfma_f32_32x32x16_bf16 v[68:83], v[136:139], v[152:155], v[68:83]
	ds_read_b64_tr_b16 v[152:153], v0 offset:0x2800
	ds_read_b64_tr_b16 v[154:155], v0 offset:0x3800
	v_mfma_f32_32x32x16_bf16 v[68:83], v[140:143], v[156:159], v[68:83]
	ds_read_b64_tr_b16 v[156:157], v0 offset:0x4800
	ds_read_b64_tr_b16 v[158:159], v0 offset:0x5800
	v_mfma_f32_32x32x16_bf16 v[68:83], v[144:147], v[160:163], v[68:83]
	ds_read_b64_tr_b16 v[160:161], v0 offset:0x6800
	ds_read_b64_tr_b16 v[162:163], v0 offset:0x7800
	s_waitcnt lgkmcnt(0)
	v_mfma_f32_32x32x16_bf16 v[52:67], v[132:135], v[148:151], v[52:67]
	ds_read_b64_tr_b16 v[148:149], v0 offset:0xa00
	ds_read_b64_tr_b16 v[150:151], v0 offset:0x1a00
	v_mfma_f32_32x32x16_bf16 v[52:67], v[136:139], v[152:155], v[52:67]
	ds_read_b64_tr_b16 v[152:153], v0 offset:0x2a00
	ds_read_b64_tr_b16 v[154:155], v0 offset:0x3a00
	v_mfma_f32_32x32x16_bf16 v[52:67], v[140:143], v[156:159], v[52:67]
	ds_read_b64_tr_b16 v[156:157], v0 offset:0x4a00
	ds_read_b64_tr_b16 v[158:159], v0 offset:0x5a00
	v_mfma_f32_32x32x16_bf16 v[52:67], v[144:147], v[160:163], v[52:67]
	ds_read_b64_tr_b16 v[160:161], v0 offset:0x6a00
	ds_read_b64_tr_b16 v[162:163], v0 offset:0x7a00
	s_waitcnt lgkmcnt(0)
	v_mfma_f32_32x32x16_bf16 v[36:51], v[132:135], v[148:151], v[36:51]
	ds_read_b64_tr_b16 v[148:149], v0 offset:0xc00
	ds_read_b64_tr_b16 v[150:151], v0 offset:0x1c00
	v_mfma_f32_32x32x16_bf16 v[36:51], v[136:139], v[152:155], v[36:51]
	ds_read_b64_tr_b16 v[152:153], v0 offset:0x2c00
	ds_read_b64_tr_b16 v[154:155], v0 offset:0x3c00
	v_mfma_f32_32x32x16_bf16 v[36:51], v[140:143], v[156:159], v[36:51]
	ds_read_b64_tr_b16 v[156:157], v0 offset:0x4c00
	ds_read_b64_tr_b16 v[158:159], v0 offset:0x5c00
	v_mfma_f32_32x32x16_bf16 v[36:51], v[144:147], v[160:163], v[36:51]
	ds_read_b64_tr_b16 v[160:161], v0 offset:0x6c00
	ds_read_b64_tr_b16 v[162:163], v0 offset:0x7c00
	s_waitcnt lgkmcnt(0)
	v_mfma_f32_32x32x16_bf16 v[20:35], v[132:135], v[148:151], v[20:35]
	ds_read_b64_tr_b16 v[148:149], v0 offset:0xe00
	ds_read_b64_tr_b16 v[150:151], v0 offset:0x1e00
	v_mfma_f32_32x32x16_bf16 v[20:35], v[136:139], v[152:155], v[20:35]
	ds_read_b64_tr_b16 v[152:153], v0 offset:0x2e00
	ds_read_b64_tr_b16 v[154:155], v0 offset:0x3e00
	v_mfma_f32_32x32x16_bf16 v[20:35], v[140:143], v[156:159], v[20:35]
	ds_read_b64_tr_b16 v[156:157], v0 offset:0x4e00
	ds_read_b64_tr_b16 v[158:159], v0 offset:0x5e00
	v_mfma_f32_32x32x16_bf16 v[20:35], v[144:147], v[160:163], v[20:35]
	ds_read_b64_tr_b16 v[160:161], v0 offset:0x6e00
	ds_read_b64_tr_b16 v[162:163], v0 offset:0x7e00
	s_waitcnt lgkmcnt(0)
	v_mfma_f32_32x32x16_bf16 v[4:19], v[132:135], v[148:151], v[4:19]
	s_and_b64 vcc, exec, s[8:9]
	v_mfma_f32_32x32x16_bf16 v[4:19], v[136:139], v[152:155], v[4:19]
	v_mfma_f32_32x32x16_bf16 v[4:19], v[140:143], v[156:159], v[4:19]
	v_mfma_f32_32x32x16_bf16 v[4:19], v[144:147], v[160:163], v[4:19]
	s_cbranch_vccnz .LBB0_944
	s_waitcnt vmcnt(0)
	v_add_u32_e32 v0, s99, v241
	s_waitcnt vmcnt(1)
	ds_write_b128 v0, v[204:207] offset:16384
	s_waitcnt vmcnt(0)
	ds_write_b128 v0, v[208:211] offset:18432
; #define SBAR() __builtin_amdgcn_sched_barrier(0)
; __device__ __forceinline__ int crow(int r, int hi) { return (r & 3) + 8 * (r >> 2) + 4 * hi; }
; #define SLOAD_A(k0) do { const bf16_t* vp_ = Vh + (long)(k0) * LDK + toff; const bf16_t* kp_ = Kh + (long)(k0) * LDK + toff; \
;     sa0 = *(const bf16x8*)kp_; sa1 = *(const bf16x8*)(kp_ + 32L * LDK); sa2 = *(const bf16x8*)vp_; sa3 = *(const bf16x8*)(vp_ + 128); } while (0)
; #define SWRITE_A(b) do { LAS char* vb_ = V_lds + (b) * SHM_V2 + vst00; LAS char* kb_ = K_lds + (b) * SHM_K2 + kst0; \
;     *(LAS bf16x8*)(kb_) = sa0; *(LAS bf16x8*)(kb_ + 8192) = sa1; *(LAS bf16x8*)(vb_) = sa2; *(LAS bf16x8*)(vb_ + 2048) = sa3; } while (0)
; #define SLOAD_B(k0) do { const bf16_t* vp_ = Vh + (long)((k0) + 32) * LDK + toff; sa0 = *(const bf16x8*)vp_; sa1 = *(const bf16x8*)(vp_ + 128); } while (0)
; #define SWRITE_B(b) do { LAS char* vb_ = V_lds + (b) * SHM_V2 + vst00; *(LAS bf16x8*)(vb_ + 16384) = sa0; *(LAS bf16x8*)(vb_ + 18432) = sa1; } while (0)
; template <int LDQ, int LDK, int LDO>
; __device__ __forceinline__ void attn_body256(const bf16_t* __restrict__ Qb, const bf16_t* __restrict__ Kh, const bf16_t* __restrict__ Vh, float* __restrict__ Ob, int seq, LAS char* lds) {
;     ...
;     if (j + 1 < NT) SLOAD_A((j + 1) * KVBLK);
;     SBAR(); qkt(p0, p1, K_lds + (j & 1) * SHM_K2, qr, r32, hi);
;     partialSM(p0, p1, m_reg, mn, al);
;     finishSM(p0, p1, al, l_reg, pa0, pa1, pa2, pa3); SBAR();
;     if (j + 1 < NT) { asm volatile("s_waitcnt vmcnt(0)" ::: "memory"); SWRITE_A((j + 1) & 1); SLOAD_B((j + 1) * KVBLK); }
;     SBAR();
;     if (__any(al < 1.f)) { if (hi == 0) al_l[r32] = al; asm volatile("s_waitcnt lgkmcnt(0)" ::: "memory");
; #pragma unroll
;       for (int d = 0; d < 8; ++d)
; #pragma unroll
;         for (int r = 0; r < 16; ++r) o[d][r] *= al_l[crow(r, hi)]; }
;     ...
;     if (j + 1 < NT) { asm volatile("s_waitcnt vmcnt(0)" ::: "memory"); SWRITE_B((j + 1) & 1); }
;     __syncthreads();
;   }
.LBB0_944:
	s_add_u32 s82, s82, 0xc2000
	v_add_f32_e32 v132, v246, v247
	s_addc_u32 s83, s83, 0
	s_add_i32 s86, s86, 0x8000
	s_mov_b32 s101, s100
	s_mov_b32 s100, s98
	s_mov_b32 s98, s99
	s_mov_b32 s99, s101
	v_fmac_f32_e32 v132, v245, v220
	s_cmp_eq_u32 s82, 0x1840000
	s_waitcnt lgkmcnt(0)
	s_barrier
	s_cbranch_scc1 .LBB0_946
	s_mov_b32 s10, s87
	v_mov_b32_e32 v248, v2
	v_mov_b32_e32 v245, v132
	s_branch .LBB0_934
.Lattn_b_top:
	s_cmp_lg_u32 s82, 0x177e000
	s_cselect_b64 s[84:85], -1, 0
	s_cmp_eq_u32 s82, 0x177e000
	v_lshl_add_u64 v[220:221], v[216:217], 0, s[82:83]
	s_cbranch_scc1 .Lattn_b_936
	v_lshl_add_u64 v[148:149], v[218:219], 0, s[82:83]
	v_add_co_u32_e32 v150, vcc, 0xc3000, v148
	s_nop 1
	v_addc_co_u32_e32 v151, vcc, 0, v149, vcc
	v_add_co_u32_e32 v148, vcc, 0x124000, v148
	s_nop 1
	v_addc_co_u32_e32 v149, vcc, 0, v149, vcc
	global_load_dwordx4 v[204:207], v[150:151], off
	global_load_dwordx4 v[208:211], v[148:149], off
	v_add_co_u32_e32 v148, vcc, 0xc4000, v220
	s_nop 1
	v_addc_co_u32_e32 v149, vcc, 0, v221, vcc
	global_load_dwordx4 v[196:199], v[148:149], off
	global_load_dwordx4 v[200:203], v[148:149], off offset:256
.Lattn_b_936:
	s_add_i32 s87, s10, 1
	s_and_b32 s88, s10, 1
	s_cmp_eq_u32 s10, 0
	s_cbranch_scc1 .Lattn_b_nopv
	v_cmp_gt_f32_e32 vcc, 1.0, v227
	s_cbranch_vccz .Lattn_b_942a
	s_and_saveexec_b64 s[10:11], s[6:7]
	ds_write_b32 v243, v227 offset:128
	s_or_b64 exec, exec, s[10:11]
	s_waitcnt lgkmcnt(0)
	v_add_u32_e32 v0, v232, v212
	ds_read_b128 v[160:163], v0 offset:224
	ds_read_b128 v[156:159], v0 offset:192
	ds_read_b128 v[152:155], v0 offset:160
	ds_read_b128 v[148:151], v0 offset:128
	s_waitcnt lgkmcnt(3)
	v_pk_mul_f32 v[128:129], v[128:129], v[160:161]
	s_waitcnt lgkmcnt(2)
	v_pk_mul_f32 v[124:125], v[124:125], v[156:157]
	s_waitcnt lgkmcnt(1)
	v_pk_mul_f32 v[120:121], v[120:121], v[152:153]
	v_pk_mul_f32 v[130:131], v[130:131], v[162:163]
	v_pk_mul_f32 v[126:127], v[126:127], v[158:159]
	v_pk_mul_f32 v[122:123], v[122:123], v[154:155]
	s_waitcnt lgkmcnt(0)
	v_pk_mul_f32 v[118:119], v[118:119], v[150:151]
	v_pk_mul_f32 v[116:117], v[116:117], v[148:149]
	v_pk_mul_f32 v[112:113], v[112:113], v[160:161]
	v_pk_mul_f32 v[108:109], v[108:109], v[156:157]
	v_pk_mul_f32 v[104:105], v[104:105], v[152:153]
	v_pk_mul_f32 v[114:115], v[114:115], v[162:163]
	v_pk_mul_f32 v[110:111], v[110:111], v[158:159]
	v_pk_mul_f32 v[106:107], v[106:107], v[154:155]
	v_pk_mul_f32 v[102:103], v[102:103], v[150:151]
	v_pk_mul_f32 v[100:101], v[100:101], v[148:149]
	v_pk_mul_f32 v[96:97], v[96:97], v[160:161]
	v_pk_mul_f32 v[92:93], v[92:93], v[156:157]
	v_pk_mul_f32 v[88:89], v[88:89], v[152:153]
	v_pk_mul_f32 v[98:99], v[98:99], v[162:163]
	v_pk_mul_f32 v[94:95], v[94:95], v[158:159]
	v_pk_mul_f32 v[90:91], v[90:91], v[154:155]
	v_pk_mul_f32 v[86:87], v[86:87], v[150:151]
	v_pk_mul_f32 v[84:85], v[84:85], v[148:149]
	v_pk_mul_f32 v[80:81], v[80:81], v[160:161]
	v_pk_mul_f32 v[76:77], v[76:77], v[156:157]
	v_pk_mul_f32 v[72:73], v[72:73], v[152:153]
	v_pk_mul_f32 v[82:83], v[82:83], v[162:163]
	v_pk_mul_f32 v[78:79], v[78:79], v[158:159]
	v_pk_mul_f32 v[74:75], v[74:75], v[154:155]
	v_pk_mul_f32 v[70:71], v[70:71], v[150:151]
	v_pk_mul_f32 v[68:69], v[68:69], v[148:149]
	v_pk_mul_f32 v[64:65], v[64:65], v[160:161]
	v_pk_mul_f32 v[60:61], v[60:61], v[156:157]
	v_pk_mul_f32 v[56:57], v[56:57], v[152:153]
	v_pk_mul_f32 v[66:67], v[66:67], v[162:163]
	v_pk_mul_f32 v[62:63], v[62:63], v[158:159]
	v_pk_mul_f32 v[58:59], v[58:59], v[154:155]
	v_pk_mul_f32 v[54:55], v[54:55], v[150:151]
	v_pk_mul_f32 v[52:53], v[52:53], v[148:149]
	v_pk_mul_f32 v[48:49], v[48:49], v[160:161]
	v_pk_mul_f32 v[44:45], v[44:45], v[156:157]
	v_pk_mul_f32 v[40:41], v[40:41], v[152:153]
	v_pk_mul_f32 v[50:51], v[50:51], v[162:163]
	v_pk_mul_f32 v[46:47], v[46:47], v[158:159]
	v_pk_mul_f32 v[42:43], v[42:43], v[154:155]
	v_pk_mul_f32 v[38:39], v[38:39], v[150:151]
	v_pk_mul_f32 v[36:37], v[36:37], v[148:149]
	v_pk_mul_f32 v[32:33], v[32:33], v[160:161]
	v_pk_mul_f32 v[28:29], v[28:29], v[156:157]
	v_pk_mul_f32 v[24:25], v[24:25], v[152:153]
	v_pk_mul_f32 v[34:35], v[34:35], v[162:163]
	v_pk_mul_f32 v[30:31], v[30:31], v[158:159]
	v_pk_mul_f32 v[26:27], v[26:27], v[154:155]
	v_pk_mul_f32 v[22:23], v[22:23], v[150:151]
	v_pk_mul_f32 v[20:21], v[20:21], v[148:149]
	v_pk_mul_f32 v[16:17], v[16:17], v[160:161]
	v_pk_mul_f32 v[12:13], v[12:13], v[156:157]
	v_pk_mul_f32 v[8:9], v[8:9], v[152:153]
	v_pk_mul_f32 v[18:19], v[18:19], v[162:163]
	v_pk_mul_f32 v[14:15], v[14:15], v[158:159]
	v_pk_mul_f32 v[10:11], v[10:11], v[154:155]
	v_pk_mul_f32 v[6:7], v[6:7], v[150:151]
	v_pk_mul_f32 v[4:5], v[4:5], v[148:149]
; #define SBAR() __builtin_amdgcn_sched_barrier(0)
; template <int D0> __device__ __forceinline__ void pv_one256(f32x16& od, int vb, bf16x8 pa0, bf16x8 pa1, bf16x8 pa2, bf16x8 pa3) {
;   const s16x4 l0 = tr_read<v_rd_off256(D0, 0, 0)>(vb), h0 = tr_read<v_rd_off256(D0, 0, 1)>(vb), l1 = tr_read<v_rd_off256(D0, 1, 0)>(vb), h1 = tr_read<v_rd_off256(D0, 1, 1)>(vb);
;   const s16x4 l2 = tr_read<v_rd_off256(D0, 2, 0)>(vb), h2 = tr_read<v_rd_off256(D0, 2, 1)>(vb), l3 = tr_read<v_rd_off256(D0, 3, 0)>(vb), h3 = tr_read<v_rd_off256(D0, 3, 1)>(vb);
;   asm volatile("s_waitcnt lgkmcnt(0)" ::: "memory"); SBAR();
;     ...
;   od = __builtin_amdgcn_mfma_f32_32x32x16_bf16(pa0, PK(l0, h0), od, 0, 0, 0);
;   od = __builtin_amdgcn_mfma_f32_32x32x16_bf16(pa1, PK(l1, h1), od, 0, 0, 0);
;   od = __builtin_amdgcn_mfma_f32_32x32x16_bf16(pa2, PK(l2, h2), od, 0, 0, 0);
;   od = __builtin_amdgcn_mfma_f32_32x32x16_bf16(pa3, PK(l3, h3), od, 0, 0, 0);
;     ...
; }
; template <int LDQ, int LDK, int LDO>
; __device__ __forceinline__ void attn_body256(const bf16_t* __restrict__ Qb, const bf16_t* __restrict__ Kh, const bf16_t* __restrict__ Vh, float* __restrict__ Ob, int seq, LAS char* lds) {
;     ...
;     { const int vb = vb0 + (j & 1) * SHM_V2;
;       pv_one256<0>(o[0], vb, pa0, pa1, pa2, pa3); pv_one256<1>(o[1], vb, pa0, pa1, pa2, pa3); pv_one256<2>(o[2], vb, pa0, pa1, pa2, pa3); pv_one256<3>(o[3], vb, pa0, pa1, pa2, pa3);
;       pv_one256<4>(o[4], vb, pa0, pa1, pa2, pa3); pv_one256<5>(o[5], vb, pa0, pa1, pa2, pa3); pv_one256<6>(o[6], vb, pa0, pa1, pa2, pa3); pv_one256<7>(o[7], vb, pa0, pa1, pa2, pa3); }
.Lattn_b_942a:
	v_add_u32_e32 v0, s100, v244
	ds_read_b64_tr_b16 v[148:149], v0 offset:0
	ds_read_b64_tr_b16 v[150:151], v0 offset:0x1000
	ds_read_b64_tr_b16 v[152:153], v0 offset:0x2000
	ds_read_b64_tr_b16 v[154:155], v0 offset:0x3000
	ds_read_b64_tr_b16 v[156:157], v0 offset:0x4000
	ds_read_b64_tr_b16 v[158:159], v0 offset:0x5000
	ds_read_b64_tr_b16 v[160:161], v0 offset:0x6000
	ds_read_b64_tr_b16 v[162:163], v0 offset:0x7000
	s_waitcnt lgkmcnt(0)
	s_nop 0
	v_mfma_f32_32x32x16_bf16 v[116:131], v[132:135], v[148:151], v[116:131]
	ds_read_b64_tr_b16 v[148:149], v0 offset:0x200
	ds_read_b64_tr_b16 v[150:151], v0 offset:0x1200
	v_mfma_f32_32x32x16_bf16 v[116:131], v[136:139], v[152:155], v[116:131]
	ds_read_b64_tr_b16 v[152:153], v0 offset:0x2200
	ds_read_b64_tr_b16 v[154:155], v0 offset:0x3200
	v_mfma_f32_32x32x16_bf16 v[116:131], v[140:143], v[156:159], v[116:131]
	ds_read_b64_tr_b16 v[156:157], v0 offset:0x4200
	ds_read_b64_tr_b16 v[158:159], v0 offset:0x5200
	v_mfma_f32_32x32x16_bf16 v[116:131], v[144:147], v[160:163], v[116:131]
	ds_read_b64_tr_b16 v[160:161], v0 offset:0x6200
	ds_read_b64_tr_b16 v[162:163], v0 offset:0x7200
	s_waitcnt lgkmcnt(0)
	v_mfma_f32_32x32x16_bf16 v[100:115], v[132:135], v[148:151], v[100:115]
	ds_read_b64_tr_b16 v[148:149], v0 offset:0x400
	ds_read_b64_tr_b16 v[150:151], v0 offset:0x1400
	v_mfma_f32_32x32x16_bf16 v[100:115], v[136:139], v[152:155], v[100:115]
	ds_read_b64_tr_b16 v[152:153], v0 offset:0x2400
	ds_read_b64_tr_b16 v[154:155], v0 offset:0x3400
	v_mfma_f32_32x32x16_bf16 v[100:115], v[140:143], v[156:159], v[100:115]
	ds_read_b64_tr_b16 v[156:157], v0 offset:0x4400
	ds_read_b64_tr_b16 v[158:159], v0 offset:0x5400
	v_mfma_f32_32x32x16_bf16 v[100:115], v[144:147], v[160:163], v[100:115]
	ds_read_b64_tr_b16 v[160:161], v0 offset:0x6400
	ds_read_b64_tr_b16 v[162:163], v0 offset:0x7400
	s_waitcnt lgkmcnt(0)
	v_mfma_f32_32x32x16_bf16 v[84:99], v[132:135], v[148:151], v[84:99]
	ds_read_b64_tr_b16 v[148:149], v0 offset:0x600
	ds_read_b64_tr_b16 v[150:151], v0 offset:0x1600
	v_mfma_f32_32x32x16_bf16 v[84:99], v[136:139], v[152:155], v[84:99]
	ds_read_b64_tr_b16 v[152:153], v0 offset:0x2600
	ds_read_b64_tr_b16 v[154:155], v0 offset:0x3600
	v_mfma_f32_32x32x16_bf16 v[84:99], v[140:143], v[156:159], v[84:99]
	ds_read_b64_tr_b16 v[156:157], v0 offset:0x4600
	ds_read_b64_tr_b16 v[158:159], v0 offset:0x5600
	v_mfma_f32_32x32x16_bf16 v[84:99], v[144:147], v[160:163], v[84:99]
	ds_read_b64_tr_b16 v[160:161], v0 offset:0x6600
	ds_read_b64_tr_b16 v[162:163], v0 offset:0x7600
	s_waitcnt lgkmcnt(0)
	v_mfma_f32_32x32x16_bf16 v[68:83], v[132:135], v[148:151], v[68:83]
	ds_read_b64_tr_b16 v[148:149], v0 offset:0x800
	ds_read_b64_tr_b16 v[150:151], v0 offset:0x1800
	v_mfma_f32_32x32x16_bf16 v[68:83], v[136:139], v[152:155], v[68:83]
	ds_read_b64_tr_b16 v[152:153], v0 offset:0x2800
	ds_read_b64_tr_b16 v[154:155], v0 offset:0x3800
	v_mfma_f32_32x32x16_bf16 v[68:83], v[140:143], v[156:159], v[68:83]
	ds_read_b64_tr_b16 v[156:157], v0 offset:0x4800
	ds_read_b64_tr_b16 v[158:159], v0 offset:0x5800
	v_mfma_f32_32x32x16_bf16 v[68:83], v[144:147], v[160:163], v[68:83]
	ds_read_b64_tr_b16 v[160:161], v0 offset:0x6800
	ds_read_b64_tr_b16 v[162:163], v0 offset:0x7800
	s_waitcnt lgkmcnt(0)
	v_mfma_f32_32x32x16_bf16 v[52:67], v[132:135], v[148:151], v[52:67]
	ds_read_b64_tr_b16 v[148:149], v0 offset:0xa00
	ds_read_b64_tr_b16 v[150:151], v0 offset:0x1a00
	v_mfma_f32_32x32x16_bf16 v[52:67], v[136:139], v[152:155], v[52:67]
	ds_read_b64_tr_b16 v[152:153], v0 offset:0x2a00
	ds_read_b64_tr_b16 v[154:155], v0 offset:0x3a00
	v_mfma_f32_32x32x16_bf16 v[52:67], v[140:143], v[156:159], v[52:67]
	ds_read_b64_tr_b16 v[156:157], v0 offset:0x4a00
	ds_read_b64_tr_b16 v[158:159], v0 offset:0x5a00
	v_mfma_f32_32x32x16_bf16 v[52:67], v[144:147], v[160:163], v[52:67]
	ds_read_b64_tr_b16 v[160:161], v0 offset:0x6a00
	ds_read_b64_tr_b16 v[162:163], v0 offset:0x7a00
	s_waitcnt lgkmcnt(0)
	v_mfma_f32_32x32x16_bf16 v[36:51], v[132:135], v[148:151], v[36:51]
	ds_read_b64_tr_b16 v[148:149], v0 offset:0xc00
	ds_read_b64_tr_b16 v[150:151], v0 offset:0x1c00
	v_mfma_f32_32x32x16_bf16 v[36:51], v[136:139], v[152:155], v[36:51]
	ds_read_b64_tr_b16 v[152:153], v0 offset:0x2c00
	ds_read_b64_tr_b16 v[154:155], v0 offset:0x3c00
	v_mfma_f32_32x32x16_bf16 v[36:51], v[140:143], v[156:159], v[36:51]
	ds_read_b64_tr_b16 v[156:157], v0 offset:0x4c00
	ds_read_b64_tr_b16 v[158:159], v0 offset:0x5c00
	v_mfma_f32_32x32x16_bf16 v[36:51], v[144:147], v[160:163], v[36:51]
	ds_read_b64_tr_b16 v[160:161], v0 offset:0x6c00
	ds_read_b64_tr_b16 v[162:163], v0 offset:0x7c00
	s_waitcnt lgkmcnt(0)
	v_mfma_f32_32x32x16_bf16 v[20:35], v[132:135], v[148:151], v[20:35]
	ds_read_b64_tr_b16 v[148:149], v0 offset:0xe00
	ds_read_b64_tr_b16 v[150:151], v0 offset:0x1e00
	v_mfma_f32_32x32x16_bf16 v[20:35], v[136:139], v[152:155], v[20:35]
	ds_read_b64_tr_b16 v[152:153], v0 offset:0x2e00
	ds_read_b64_tr_b16 v[154:155], v0 offset:0x3e00
	v_mfma_f32_32x32x16_bf16 v[20:35], v[140:143], v[156:159], v[20:35]
	ds_read_b64_tr_b16 v[156:157], v0 offset:0x4e00
	ds_read_b64_tr_b16 v[158:159], v0 offset:0x5e00
	v_mfma_f32_32x32x16_bf16 v[20:35], v[144:147], v[160:163], v[20:35]
	ds_read_b64_tr_b16 v[160:161], v0 offset:0x6e00
	ds_read_b64_tr_b16 v[162:163], v0 offset:0x7e00
	s_waitcnt lgkmcnt(0)
	v_mfma_f32_32x32x16_bf16 v[4:19], v[132:135], v[148:151], v[4:19]
	v_mfma_f32_32x32x16_bf16 v[4:19], v[136:139], v[152:155], v[4:19]
	v_mfma_f32_32x32x16_bf16 v[4:19], v[140:143], v[156:159], v[4:19]
	v_mfma_f32_32x32x16_bf16 v[4:19], v[144:147], v[160:163], v[4:19]
; #define LAS __attribute__((address_space(3)))
; #define SWRITE_A(b) do { LAS char* vb_ = V_lds + (b) * SHM_V2 + vst00; LAS char* kb_ = K_lds + (b) * SHM_K2 + kst0; \
;     *(LAS bf16x8*)(kb_) = sa0; *(LAS bf16x8*)(kb_ + 8192) = sa1; *(LAS bf16x8*)(vb_) = sa2; *(LAS bf16x8*)(vb_ + 2048) = sa3; } while (0)
; #define SLOAD_B(k0) do { const bf16_t* vp_ = Vh + (long)((k0) + 32) * LDK + toff; sa0 = *(const bf16x8*)vp_; sa1 = *(const bf16x8*)(vp_ + 128); } while (0)
; __device__ __forceinline__ void partialSM(f32x16& p0, f32x16& p1, float& m_reg, float& mn, float& alpha) {
;   constexpr float C = SCALE * 1.4426950408889634f;
;   float pmax = p0[0]; for (int r = 1; r < 16; ++r) pmax = fmaxf(pmax, p0[r]); for (int r = 0; r < 16; ++r) pmax = fmaxf(pmax, p1[r]);
;   { auto rr = __builtin_amdgcn_permlane32_swap(__float_as_uint(pmax), __float_as_uint(pmax), false, false);
;     pmax = fmaxf(__uint_as_float(rr[0]), __uint_as_float(rr[1])); }
;   if (__builtin_expect(__all(pmax - m_reg <= THR / SCALE), 1)) { mn = m_reg; alpha = 1.f; }
;   else { mn = fmaxf(m_reg, pmax); alpha = __builtin_amdgcn_exp2f((m_reg - mn) * C); m_reg = mn; }
;   float mnC = -mn * C;
;   for (int r = 0; r < 16; ++r) p0[r] = fmaf(p0[r], C, mnC); for (int r = 0; r < 16; ++r) p1[r] = fmaf(p1[r], C, mnC);
;   for (int r = 0; r < 16; ++r) p0[r] = __builtin_amdgcn_exp2f(p0[r]);
; __device__ __forceinline__ void qkt(f32x16& p0, f32x16& p1, const LAS char* Ks, const bf16x8* qr, int r32, int hi) {
;   p0 = f32x16{}; p1 = f32x16{};
; #pragma unroll
;   for (int d0 = 0; d0 < 8; ++d0) { int cb = (d0 * 16 + hi * 8) * 2;
;     bf16x8 b0 = *(const LAS bf16x8*)(Ks + KSWZ(r32, cb));
;     bf16x8 b1 = *(const LAS bf16x8*)(Ks + KSWZ(32 + r32, cb));
;     p0 = __builtin_amdgcn_mfma_f32_32x32x16_bf16(b0, qr[d0], p0, 0, 0, 0);
;     p1 = __builtin_amdgcn_mfma_f32_32x32x16_bf16(b1, qr[d0], p1, 0, 0, 0); }
; }
; template <int LDQ, int LDK, int LDO>
; __device__ __forceinline__ void attn_body256(const bf16_t* __restrict__ Qb, const bf16_t* __restrict__ Kh, const bf16_t* __restrict__ Vh, float* __restrict__ Ob, int seq, LAS char* lds) {
;     ...
;     if (j + 1 < NT) { asm volatile("s_waitcnt vmcnt(0)" ::: "memory"); SWRITE_A((j + 1) & 1); SLOAD_B((j + 1) * KVBLK); }
.Lattn_b_nopv:
	v_cndmask_b32_e64 v0, 0, 1, s[84:85]
	v_cmp_ne_u32_e64 s[8:9], 1, v0
	s_andn2_b64 vcc, exec, s[84:85]
	s_cbranch_vccnz .Lattn_b_938
	s_and_b32 s84, s87, 1
	v_lshl_add_u32 v1, s84, 14, v240
	v_add_co_u32_e32 v148, vcc, 0x125000, v220
	s_waitcnt vmcnt(0)
	v_add_u32_e32 v0, s99, v241
	s_waitcnt vmcnt(1)
	ds_write_b128 v1, v[204:207]
	s_waitcnt vmcnt(0)
	ds_write_b128 v1, v[208:211] offset:8192
	s_waitcnt vmcnt(1)
	ds_write_b128 v0, v[196:199]
	s_waitcnt vmcnt(0)
	ds_write_b128 v0, v[200:203] offset:2048
	v_addc_co_u32_e32 v149, vcc, 0, v221, vcc
	global_load_dwordx4 v[204:207], v[148:149], off
	global_load_dwordx4 v[208:211], v[148:149], off offset:256
.Lattn_b_938:
	v_lshl_add_u32 v2, s88, 14, v239
	v_add_u32_e32 v136, v2, v215
	ds_read_b128 v[132:135], v136
	ds_read_b128 v[136:139], v136 offset:8192
	v_add_u32_e32 v222, v2, v233
	ds_read_b128 v[250:253], v222
	ds_read_b128 v[222:225], v222 offset:8192
	v_add_u32_e32 v246, v2, v234
	s_waitcnt lgkmcnt(3)
	v_mfma_f32_32x32x16_bf16 v[148:163], v[132:135], v[164:167], 0
	s_mov_b32 s8, 0x42b504f3
	s_waitcnt lgkmcnt(2)
	v_mfma_f32_32x32x16_bf16 v[132:147], v[136:139], v[164:167], 0
	s_waitcnt lgkmcnt(1)
	v_mfma_f32_32x32x16_bf16 v[148:163], v[250:253], v[168:171], v[148:163]
	s_waitcnt lgkmcnt(0)
	v_mfma_f32_32x32x16_bf16 v[132:147], v[222:225], v[168:171], v[132:147]
	ds_read_b128 v[222:225], v246
	ds_read_b128 v[250:253], v246 offset:8192
	v_add_u32_e32 v246, v2, v235
	s_waitcnt lgkmcnt(1)
	v_mfma_f32_32x32x16_bf16 v[148:163], v[222:225], v[172:175], v[148:163]
	s_waitcnt lgkmcnt(0)
	v_mfma_f32_32x32x16_bf16 v[132:147], v[250:253], v[172:175], v[132:147]
	ds_read_b128 v[222:225], v246
	ds_read_b128 v[250:253], v246 offset:8192
	v_add_u32_e32 v246, v2, v236
	s_waitcnt lgkmcnt(1)
	v_mfma_f32_32x32x16_bf16 v[148:163], v[222:225], v[176:179], v[148:163]
	s_waitcnt lgkmcnt(0)
	v_mfma_f32_32x32x16_bf16 v[132:147], v[250:253], v[176:179], v[132:147]
	ds_read_b128 v[222:225], v246
	ds_read_b128 v[250:253], v246 offset:8192
	v_add_u32_e32 v246, v2, v237
	s_waitcnt lgkmcnt(1)
	v_mfma_f32_32x32x16_bf16 v[148:163], v[222:225], v[180:183], v[148:163]
	s_waitcnt lgkmcnt(0)
	v_mfma_f32_32x32x16_bf16 v[132:147], v[250:253], v[180:183], v[132:147]
	ds_read_b128 v[222:225], v246
	ds_read_b128 v[250:253], v246 offset:8192
	v_add_u32_e32 v246, v2, v238
	v_add_u32_e32 v2, v2, v242
	s_waitcnt lgkmcnt(1)
	v_mfma_f32_32x32x16_bf16 v[148:163], v[222:225], v[184:187], v[148:163]
	s_waitcnt lgkmcnt(0)
	v_mfma_f32_32x32x16_bf16 v[132:147], v[250:253], v[184:187], v[132:147]
	ds_read_b128 v[222:225], v246
	ds_read_b128 v[250:253], v246 offset:8192
	s_waitcnt lgkmcnt(1)
	v_mfma_f32_32x32x16_bf16 v[148:163], v[222:225], v[188:191], v[148:163]
	s_waitcnt lgkmcnt(0)
	v_mfma_f32_32x32x16_bf16 v[132:147], v[250:253], v[188:191], v[132:147]
	ds_read_b128 v[222:225], v2
	ds_read_b128 v[250:253], v2 offset:8192
	s_waitcnt lgkmcnt(1)
	v_mfma_f32_32x32x16_bf16 v[148:163], v[222:225], v[192:195], v[148:163]
	s_waitcnt lgkmcnt(0)
	v_mfma_f32_32x32x16_bf16 v[132:147], v[250:253], v[192:195], v[132:147]
	s_nop 9
	v_max_f32_e32 v2, v149, v149
	v_max_f32_e32 v222, v148, v148
	v_max_f32_e32 v2, v222, v2
	v_max3_f32 v2, v2, v150, v151
	v_max3_f32 v2, v2, v152, v153
	v_max3_f32 v2, v2, v154, v155
	v_max3_f32 v2, v2, v156, v157
	v_max3_f32 v2, v2, v158, v159
	v_max3_f32 v2, v2, v160, v161
	v_max3_f32 v2, v2, v162, v163
	v_max3_f32 v2, v2, v132, v133
	v_max3_f32 v2, v2, v134, v135
	v_max3_f32 v2, v2, v136, v137
	v_max3_f32 v2, v2, v138, v139
	v_max3_f32 v2, v2, v140, v141
	v_max3_f32 v2, v2, v142, v143
	v_max3_f32 v2, v2, v144, v145
	v_max3_f32 v2, v2, v146, v147
	v_mov_b32_e32 v222, v2
	s_nop 1
	v_permlane32_swap_b32_e32 v2, v222
	v_max_f32_e32 v222, v222, v222
	v_max_f32_e32 v2, v2, v2
	v_max_f32_e32 v2, v2, v222
	v_sub_f32_e32 v222, v2, v248
	v_cmp_ge_f32_e32 vcc, s8, v222
	s_cmp_eq_u64 vcc, exec
	v_max_f32_e32 v222, v248, v248
	s_cselect_b64 s[10:11], -1, 0
	v_max_f32_e32 v249, v222, v2
	v_cndmask_b32_e64 v2, v249, v248, s[10:11]
	v_mul_f32_e32 v222, 0xbe0293ee, v2
	v_fmamk_f32 v148, v148, 0x3e0293ee, v222
	v_fmamk_f32 v149, v149, 0x3e0293ee, v222
	v_fmamk_f32 v150, v150, 0x3e0293ee, v222
	v_fmamk_f32 v151, v151, 0x3e0293ee, v222
	v_fmamk_f32 v152, v152, 0x3e0293ee, v222
	v_fmamk_f32 v153, v153, 0x3e0293ee, v222
	v_fmamk_f32 v154, v154, 0x3e0293ee, v222
	v_fmamk_f32 v155, v155, 0x3e0293ee, v222
	v_fmamk_f32 v156, v156, 0x3e0293ee, v222
	v_fmamk_f32 v157, v157, 0x3e0293ee, v222
	v_fmamk_f32 v158, v158, 0x3e0293ee, v222
	v_fmamk_f32 v159, v159, 0x3e0293ee, v222
	v_fmamk_f32 v160, v160, 0x3e0293ee, v222
	v_fmamk_f32 v161, v161, 0x3e0293ee, v222
	v_fmamk_f32 v162, v162, 0x3e0293ee, v222
	v_fmamk_f32 v163, v163, 0x3e0293ee, v222
	v_fmamk_f32 v132, v132, 0x3e0293ee, v222
	v_fmamk_f32 v133, v133, 0x3e0293ee, v222
	v_fmamk_f32 v134, v134, 0x3e0293ee, v222
	v_fmamk_f32 v135, v135, 0x3e0293ee, v222
	v_fmamk_f32 v136, v136, 0x3e0293ee, v222
	v_fmamk_f32 v137, v137, 0x3e0293ee, v222
	v_fmamk_f32 v138, v138, 0x3e0293ee, v222
	v_fmamk_f32 v139, v139, 0x3e0293ee, v222
	v_fmamk_f32 v140, v140, 0x3e0293ee, v222
	v_fmamk_f32 v141, v141, 0x3e0293ee, v222
	v_fmamk_f32 v142, v142, 0x3e0293ee, v222
	v_fmamk_f32 v143, v143, 0x3e0293ee, v222
	v_fmamk_f32 v144, v144, 0x3e0293ee, v222
	v_fmamk_f32 v145, v145, 0x3e0293ee, v222
	v_fmamk_f32 v146, v146, 0x3e0293ee, v222
	v_fmac_f32_e32 v222, 0x3e0293ee, v147
	v_exp_f32_e32 v147, v148
	v_exp_f32_e32 v148, v149
	v_exp_f32_e32 v149, v150
	v_exp_f32_e32 v150, v151
	v_exp_f32_e32 v151, v152
	v_exp_f32_e32 v152, v153
	v_exp_f32_e32 v153, v154
	v_exp_f32_e32 v154, v155
	v_exp_f32_e32 v155, v156
; __device__ __forceinline__ int crow(int r, int hi) { return (r & 3) + 8 * (r >> 2) + 4 * hi; }
; #define SWRITE_B(b) do { LAS char* vb_ = V_lds + (b) * SHM_V2 + vst00; *(LAS bf16x8*)(vb_ + 16384) = sa0; *(LAS bf16x8*)(vb_ + 18432) = sa1; } while (0)
; __device__ __forceinline__ void finishSM(f32x16& p0, f32x16& p1, float alpha, float& l_reg, bf16x8& pa0, bf16x8& pa1, bf16x8& pa2, bf16x8& pa3) {
;   for (int r = 0; r < 16; ++r) p1[r] = __builtin_amdgcn_exp2f(p1[r]);
;   float ps = 0; for (int r = 0; r < 16; ++r) ps += p0[r]; for (int r = 0; r < 16; ++r) ps += p1[r];
;   { auto rr = __builtin_amdgcn_permlane32_swap(__float_as_uint(ps), __float_as_uint(ps), false, false);
;     ps = __uint_as_float(rr[0]) + __uint_as_float(rr[1]); }
;   l_reg = l_reg * alpha + ps;
;     ...
;   PK4(p0, 0, pa0); PK4(p0, 8, pa1); PK4(p1, 0, pa2); PK4(p1, 8, pa3);
; template <int LDQ, int LDK, int LDO>
; __device__ __forceinline__ void attn_body256(const bf16_t* __restrict__ Qb, const bf16_t* __restrict__ Kh, const bf16_t* __restrict__ Vh, float* __restrict__ Ob, int seq, LAS char* lds) {
;     ...
;     if (__any(al < 1.f)) { if (hi == 0) al_l[r32] = al; asm volatile("s_waitcnt lgkmcnt(0)" ::: "memory");
; #pragma unroll
;       for (int d = 0; d < 8; ++d)
; #pragma unroll
;         for (int r = 0; r < 16; ++r) o[d][r] *= al_l[crow(r, hi)]; }
;     { const int vb = vb0 + (j & 1) * SHM_V2;
;       pv_one256<0>(o[0], vb, pa0, pa1, pa2, pa3); pv_one256<1>(o[1], vb, pa0, pa1, pa2, pa3); pv_one256<2>(o[2], vb, pa0, pa1, pa2, pa3); pv_one256<3>(o[3], vb, pa0, pa1, pa2, pa3);
;       pv_one256<4>(o[4], vb, pa0, pa1, pa2, pa3); pv_one256<5>(o[5], vb, pa0, pa1, pa2, pa3); pv_one256<6>(o[6], vb, pa0, pa1, pa2, pa3); pv_one256<7>(o[7], vb, pa0, pa1, pa2, pa3); }
;     if (j + 1 < NT) { asm volatile("s_waitcnt vmcnt(0)" ::: "memory"); SWRITE_B((j + 1) & 1); }
;     __syncthreads();
;   }
	v_exp_f32_e32 v156, v157
	v_exp_f32_e32 v157, v158
	v_exp_f32_e32 v158, v159
	v_exp_f32_e32 v159, v160
	v_exp_f32_e32 v160, v161
	v_exp_f32_e32 v161, v162
	v_exp_f32_e32 v162, v163
	v_exp_f32_e32 v163, v132
	v_add_f32_e32 v132, 0, v147
	v_add_f32_e32 v132, v148, v132
	v_add_f32_e32 v132, v149, v132
	v_add_f32_e32 v132, v150, v132
	v_add_f32_e32 v132, v151, v132
	v_add_f32_e32 v132, v152, v132
	v_add_f32_e32 v132, v153, v132
	v_add_f32_e32 v132, v154, v132
	v_add_f32_e32 v132, v155, v132
	v_add_f32_e32 v132, v156, v132
	v_add_f32_e32 v132, v157, v132
	v_add_f32_e32 v132, v158, v132
	v_add_f32_e32 v132, v159, v132
	v_exp_f32_e32 v223, v133
	v_add_f32_e32 v132, v160, v132
	v_exp_f32_e32 v224, v134
	v_add_f32_e32 v132, v161, v132
	v_exp_f32_e32 v225, v135
	v_add_f32_e32 v132, v162, v132
	v_exp_f32_e32 v250, v136
	v_add_f32_e32 v132, v163, v132
	v_exp_f32_e32 v251, v137
	v_add_f32_e32 v132, v223, v132
	v_exp_f32_e32 v252, v138
	v_add_f32_e32 v132, v224, v132
	v_exp_f32_e32 v253, v139
	v_add_f32_e32 v132, v225, v132
	v_exp_f32_e32 v254, v140
	v_add_f32_e32 v132, v250, v132
	v_exp_f32_e32 v0, v141
	v_add_f32_e32 v132, v251, v132
	v_exp_f32_e32 v1, v142
	v_add_f32_e32 v132, v252, v132
	v_exp_f32_e32 v227, v143
	v_add_f32_e32 v132, v253, v132
	v_exp_f32_e32 v228, v144
	v_add_f32_e32 v132, v254, v132
	v_exp_f32_e32 v229, v145
	v_add_f32_e32 v132, v0, v132
	v_exp_f32_e32 v230, v146
	v_add_f32_e32 v132, v1, v132
	v_exp_f32_e32 v222, v222
	v_add_f32_e32 v132, v227, v132
	v_add_f32_e32 v132, v228, v132
	v_add_f32_e32 v132, v229, v132
	v_add_f32_e32 v132, v230, v132
	v_add_f32_e32 v246, v222, v132
	v_mov_b32_e32 v247, v246
	v_cvt_pk_bf16_f32 v132, v147, v148
	v_cvt_pk_bf16_f32 v133, v149, v150
	v_cvt_pk_bf16_f32 v134, v151, v152
	v_cvt_pk_bf16_f32 v135, v153, v154
	v_cvt_pk_bf16_f32 v136, v155, v156
	v_cvt_pk_bf16_f32 v137, v157, v158
	v_cvt_pk_bf16_f32 v138, v159, v160
	v_cvt_pk_bf16_f32 v139, v161, v162
	v_cvt_pk_bf16_f32 v140, v163, v223
	v_cvt_pk_bf16_f32 v141, v224, v225
	v_cvt_pk_bf16_f32 v142, v250, v251
	v_cvt_pk_bf16_f32 v143, v252, v253
	v_cvt_pk_bf16_f32 v144, v254, v0
	v_cvt_pk_bf16_f32 v145, v1, v227
	v_cvt_pk_bf16_f32 v146, v228, v229
	v_cvt_pk_bf16_f32 v147, v230, v222
	s_nop 1
	v_permlane32_swap_b32_e32 v246, v247
	v_permlane32_swap_b32_e32 v132, v134
	v_permlane32_swap_b32_e32 v133, v135
	v_permlane32_swap_b32_e32 v136, v138
	v_permlane32_swap_b32_e32 v137, v139
	v_permlane32_swap_b32_e32 v140, v142
	v_permlane32_swap_b32_e32 v141, v143
	v_permlane32_swap_b32_e32 v144, v146
	v_permlane32_swap_b32_e32 v145, v147
	v_sub_f32_e32 v0, v248, v249
	v_mul_f32_e32 v0, 0x3e0293ee, v0
	v_exp_f32_e32 v0, v0
	s_nop 0
	v_cndmask_b32_e64 v227, v0, 1.0, s[10:11]
	v_add_f32_e32 v0, v246, v247
	v_fmac_f32_e32 v0, v245, v227
	v_mov_b32_e32 v245, v0
	v_mov_b32_e32 v248, v2
	s_cmp_eq_u32 s82, 0x177e000
	s_cbranch_scc1 .Lattn_b_944
	s_waitcnt vmcnt(0)
	v_add_u32_e32 v0, s99, v241
	s_waitcnt vmcnt(1)
	ds_write_b128 v0, v[204:207] offset:16384
	s_waitcnt vmcnt(0)
	ds_write_b128 v0, v[208:211] offset:18432
.Lattn_b_944:
	s_add_u32 s82, s82, 0xc2000
	s_addc_u32 s83, s83, 0
	s_mov_b32 s101, s100
	s_mov_b32 s100, s98
	s_mov_b32 s98, s99
	s_mov_b32 s99, s101
	s_cmp_eq_u32 s82, 0x1840000
	s_waitcnt lgkmcnt(0)
	s_barrier
	s_cbranch_scc1 .Lattn_b_exit
	s_mov_b32 s10, s87
	s_branch .Lattn_b_top
.Lattn_b_exit:
	v_cmp_gt_f32_e32 vcc, 1.0, v227
	s_cbranch_vccz .Lattn_b_942b
	s_and_saveexec_b64 s[10:11], s[6:7]
	ds_write_b32 v243, v227 offset:128
	s_or_b64 exec, exec, s[10:11]
	s_waitcnt lgkmcnt(0)
	v_add_u32_e32 v0, v232, v212
	ds_read_b128 v[160:163], v0 offset:224
	ds_read_b128 v[156:159], v0 offset:192
	ds_read_b128 v[152:155], v0 offset:160
	ds_read_b128 v[148:151], v0 offset:128
	s_waitcnt lgkmcnt(3)
	v_pk_mul_f32 v[128:129], v[128:129], v[160:161]
	s_waitcnt lgkmcnt(2)
	v_pk_mul_f32 v[124:125], v[124:125], v[156:157]
	s_waitcnt lgkmcnt(1)
	v_pk_mul_f32 v[120:121], v[120:121], v[152:153]
	v_pk_mul_f32 v[130:131], v[130:131], v[162:163]
	v_pk_mul_f32 v[126:127], v[126:127], v[158:159]
	v_pk_mul_f32 v[122:123], v[122:123], v[154:155]
	s_waitcnt lgkmcnt(0)
	v_pk_mul_f32 v[118:119], v[118:119], v[150:151]
	v_pk_mul_f32 v[116:117], v[116:117], v[148:149]
	v_pk_mul_f32 v[112:113], v[112:113], v[160:161]
	v_pk_mul_f32 v[108:109], v[108:109], v[156:157]
	v_pk_mul_f32 v[104:105], v[104:105], v[152:153]
	v_pk_mul_f32 v[114:115], v[114:115], v[162:163]
	v_pk_mul_f32 v[110:111], v[110:111], v[158:159]
	v_pk_mul_f32 v[106:107], v[106:107], v[154:155]
	v_pk_mul_f32 v[102:103], v[102:103], v[150:151]
	v_pk_mul_f32 v[100:101], v[100:101], v[148:149]
	v_pk_mul_f32 v[96:97], v[96:97], v[160:161]
	v_pk_mul_f32 v[92:93], v[92:93], v[156:157]
	v_pk_mul_f32 v[88:89], v[88:89], v[152:153]
	v_pk_mul_f32 v[98:99], v[98:99], v[162:163]
	v_pk_mul_f32 v[94:95], v[94:95], v[158:159]
	v_pk_mul_f32 v[90:91], v[90:91], v[154:155]
	v_pk_mul_f32 v[86:87], v[86:87], v[150:151]
	v_pk_mul_f32 v[84:85], v[84:85], v[148:149]
	v_pk_mul_f32 v[80:81], v[80:81], v[160:161]
	v_pk_mul_f32 v[76:77], v[76:77], v[156:157]
	v_pk_mul_f32 v[72:73], v[72:73], v[152:153]
	v_pk_mul_f32 v[82:83], v[82:83], v[162:163]
	v_pk_mul_f32 v[78:79], v[78:79], v[158:159]
	v_pk_mul_f32 v[74:75], v[74:75], v[154:155]
	v_pk_mul_f32 v[70:71], v[70:71], v[150:151]
	v_pk_mul_f32 v[68:69], v[68:69], v[148:149]
	v_pk_mul_f32 v[64:65], v[64:65], v[160:161]
	v_pk_mul_f32 v[60:61], v[60:61], v[156:157]
	v_pk_mul_f32 v[56:57], v[56:57], v[152:153]
	v_pk_mul_f32 v[66:67], v[66:67], v[162:163]
	v_pk_mul_f32 v[62:63], v[62:63], v[158:159]
	v_pk_mul_f32 v[58:59], v[58:59], v[154:155]
	v_pk_mul_f32 v[54:55], v[54:55], v[150:151]
	v_pk_mul_f32 v[52:53], v[52:53], v[148:149]
	v_pk_mul_f32 v[48:49], v[48:49], v[160:161]
	v_pk_mul_f32 v[44:45], v[44:45], v[156:157]
	v_pk_mul_f32 v[40:41], v[40:41], v[152:153]
	v_pk_mul_f32 v[50:51], v[50:51], v[162:163]
	v_pk_mul_f32 v[46:47], v[46:47], v[158:159]
	v_pk_mul_f32 v[42:43], v[42:43], v[154:155]
	v_pk_mul_f32 v[38:39], v[38:39], v[150:151]
	v_pk_mul_f32 v[36:37], v[36:37], v[148:149]
	v_pk_mul_f32 v[32:33], v[32:33], v[160:161]
	v_pk_mul_f32 v[28:29], v[28:29], v[156:157]
	v_pk_mul_f32 v[24:25], v[24:25], v[152:153]
	v_pk_mul_f32 v[34:35], v[34:35], v[162:163]
	v_pk_mul_f32 v[30:31], v[30:31], v[158:159]
	v_pk_mul_f32 v[26:27], v[26:27], v[154:155]
	v_pk_mul_f32 v[22:23], v[22:23], v[150:151]
	v_pk_mul_f32 v[20:21], v[20:21], v[148:149]
	v_pk_mul_f32 v[16:17], v[16:17], v[160:161]
	v_pk_mul_f32 v[12:13], v[12:13], v[156:157]
	v_pk_mul_f32 v[8:9], v[8:9], v[152:153]
	v_pk_mul_f32 v[18:19], v[18:19], v[162:163]
	v_pk_mul_f32 v[14:15], v[14:15], v[158:159]
	v_pk_mul_f32 v[10:11], v[10:11], v[154:155]
	v_pk_mul_f32 v[6:7], v[6:7], v[150:151]
	v_pk_mul_f32 v[4:5], v[4:5], v[148:149]
; #define SWRITE_B(b) do { LAS char* vb_ = V_lds + (b) * SHM_V2 + vst00; *(LAS bf16x8*)(vb_ + 16384) = sa0; *(LAS bf16x8*)(vb_ + 18432) = sa1; } while (0)
; template <int LDQ, int LDK, int LDO>
; __device__ __forceinline__ void attn_body256(const bf16_t* __restrict__ Qb, const bf16_t* __restrict__ Kh, const bf16_t* __restrict__ Vh, float* __restrict__ Ob, int seq, LAS char* lds) {
;     ...
;     { const int vb = vb0 + (j & 1) * SHM_V2;
;       pv_one256<0>(o[0], vb, pa0, pa1, pa2, pa3); pv_one256<1>(o[1], vb, pa0, pa1, pa2, pa3); pv_one256<2>(o[2], vb, pa0, pa1, pa2, pa3); pv_one256<3>(o[3], vb, pa0, pa1, pa2, pa3);
;       pv_one256<4>(o[4], vb, pa0, pa1, pa2, pa3); pv_one256<5>(o[5], vb, pa0, pa1, pa2, pa3); pv_one256<6>(o[6], vb, pa0, pa1, pa2, pa3); pv_one256<7>(o[7], vb, pa0, pa1, pa2, pa3); }
;     if (j + 1 < NT) { asm volatile("s_waitcnt vmcnt(0)" ::: "memory"); SWRITE_B((j + 1) & 1); }
;     __syncthreads();
;   }
;   if (hi == 0) li_l[r32] = l_reg; asm volatile("s_waitcnt lgkmcnt(0)" ::: "memory");
.Lattn_b_942b:
	v_add_u32_e32 v0, s100, v244
	ds_read_b64_tr_b16 v[148:149], v0 offset:0
	ds_read_b64_tr_b16 v[150:151], v0 offset:0x1000
	ds_read_b64_tr_b16 v[152:153], v0 offset:0x2000
	ds_read_b64_tr_b16 v[154:155], v0 offset:0x3000
	ds_read_b64_tr_b16 v[156:157], v0 offset:0x4000
	ds_read_b64_tr_b16 v[158:159], v0 offset:0x5000
	ds_read_b64_tr_b16 v[160:161], v0 offset:0x6000
	ds_read_b64_tr_b16 v[162:163], v0 offset:0x7000
	s_waitcnt lgkmcnt(0)
	s_nop 0
	v_mfma_f32_32x32x16_bf16 v[116:131], v[132:135], v[148:151], v[116:131]
	ds_read_b64_tr_b16 v[148:149], v0 offset:0x200
	ds_read_b64_tr_b16 v[150:151], v0 offset:0x1200
	v_mfma_f32_32x32x16_bf16 v[116:131], v[136:139], v[152:155], v[116:131]
	ds_read_b64_tr_b16 v[152:153], v0 offset:0x2200
	ds_read_b64_tr_b16 v[154:155], v0 offset:0x3200
	v_mfma_f32_32x32x16_bf16 v[116:131], v[140:143], v[156:159], v[116:131]
	ds_read_b64_tr_b16 v[156:157], v0 offset:0x4200
	ds_read_b64_tr_b16 v[158:159], v0 offset:0x5200
	v_mfma_f32_32x32x16_bf16 v[116:131], v[144:147], v[160:163], v[116:131]
	ds_read_b64_tr_b16 v[160:161], v0 offset:0x6200
	ds_read_b64_tr_b16 v[162:163], v0 offset:0x7200
	s_waitcnt lgkmcnt(0)
	v_mfma_f32_32x32x16_bf16 v[100:115], v[132:135], v[148:151], v[100:115]
	ds_read_b64_tr_b16 v[148:149], v0 offset:0x400
	ds_read_b64_tr_b16 v[150:151], v0 offset:0x1400
	v_mfma_f32_32x32x16_bf16 v[100:115], v[136:139], v[152:155], v[100:115]
	ds_read_b64_tr_b16 v[152:153], v0 offset:0x2400
	ds_read_b64_tr_b16 v[154:155], v0 offset:0x3400
	v_mfma_f32_32x32x16_bf16 v[100:115], v[140:143], v[156:159], v[100:115]
	ds_read_b64_tr_b16 v[156:157], v0 offset:0x4400
	ds_read_b64_tr_b16 v[158:159], v0 offset:0x5400
	v_mfma_f32_32x32x16_bf16 v[100:115], v[144:147], v[160:163], v[100:115]
	ds_read_b64_tr_b16 v[160:161], v0 offset:0x6400
	ds_read_b64_tr_b16 v[162:163], v0 offset:0x7400
	s_waitcnt lgkmcnt(0)
	v_mfma_f32_32x32x16_bf16 v[84:99], v[132:135], v[148:151], v[84:99]
	ds_read_b64_tr_b16 v[148:149], v0 offset:0x600
	ds_read_b64_tr_b16 v[150:151], v0 offset:0x1600
	v_mfma_f32_32x32x16_bf16 v[84:99], v[136:139], v[152:155], v[84:99]
	ds_read_b64_tr_b16 v[152:153], v0 offset:0x2600
	ds_read_b64_tr_b16 v[154:155], v0 offset:0x3600
	v_mfma_f32_32x32x16_bf16 v[84:99], v[140:143], v[156:159], v[84:99]
	ds_read_b64_tr_b16 v[156:157], v0 offset:0x4600
	ds_read_b64_tr_b16 v[158:159], v0 offset:0x5600
	v_mfma_f32_32x32x16_bf16 v[84:99], v[144:147], v[160:163], v[84:99]
	ds_read_b64_tr_b16 v[160:161], v0 offset:0x6600
	ds_read_b64_tr_b16 v[162:163], v0 offset:0x7600
	s_waitcnt lgkmcnt(0)
	v_mfma_f32_32x32x16_bf16 v[68:83], v[132:135], v[148:151], v[68:83]
	ds_read_b64_tr_b16 v[148:149], v0 offset:0x800
	ds_read_b64_tr_b16 v[150:151], v0 offset:0x1800
	v_mfma_f32_32x32x16_bf16 v[68:83], v[136:139], v[152:155], v[68:83]
	ds_read_b64_tr_b16 v[152:153], v0 offset:0x2800
	ds_read_b64_tr_b16 v[154:155], v0 offset:0x3800
	v_mfma_f32_32x32x16_bf16 v[68:83], v[140:143], v[156:159], v[68:83]
	ds_read_b64_tr_b16 v[156:157], v0 offset:0x4800
	ds_read_b64_tr_b16 v[158:159], v0 offset:0x5800
	v_mfma_f32_32x32x16_bf16 v[68:83], v[144:147], v[160:163], v[68:83]
	ds_read_b64_tr_b16 v[160:161], v0 offset:0x6800
	ds_read_b64_tr_b16 v[162:163], v0 offset:0x7800
	s_waitcnt lgkmcnt(0)
	v_mfma_f32_32x32x16_bf16 v[52:67], v[132:135], v[148:151], v[52:67]
	ds_read_b64_tr_b16 v[148:149], v0 offset:0xa00
	ds_read_b64_tr_b16 v[150:151], v0 offset:0x1a00
	v_mfma_f32_32x32x16_bf16 v[52:67], v[136:139], v[152:155], v[52:67]
	ds_read_b64_tr_b16 v[152:153], v0 offset:0x2a00
	ds_read_b64_tr_b16 v[154:155], v0 offset:0x3a00
	v_mfma_f32_32x32x16_bf16 v[52:67], v[140:143], v[156:159], v[52:67]
	ds_read_b64_tr_b16 v[156:157], v0 offset:0x4a00
	ds_read_b64_tr_b16 v[158:159], v0 offset:0x5a00
	v_mfma_f32_32x32x16_bf16 v[52:67], v[144:147], v[160:163], v[52:67]
	ds_read_b64_tr_b16 v[160:161], v0 offset:0x6a00
	ds_read_b64_tr_b16 v[162:163], v0 offset:0x7a00
	s_waitcnt lgkmcnt(0)
	v_mfma_f32_32x32x16_bf16 v[36:51], v[132:135], v[148:151], v[36:51]
	ds_read_b64_tr_b16 v[148:149], v0 offset:0xc00
	ds_read_b64_tr_b16 v[150:151], v0 offset:0x1c00
	v_mfma_f32_32x32x16_bf16 v[36:51], v[136:139], v[152:155], v[36:51]
	ds_read_b64_tr_b16 v[152:153], v0 offset:0x2c00
	ds_read_b64_tr_b16 v[154:155], v0 offset:0x3c00
	v_mfma_f32_32x32x16_bf16 v[36:51], v[140:143], v[156:159], v[36:51]
	ds_read_b64_tr_b16 v[156:157], v0 offset:0x4c00
	ds_read_b64_tr_b16 v[158:159], v0 offset:0x5c00
	v_mfma_f32_32x32x16_bf16 v[36:51], v[144:147], v[160:163], v[36:51]
	ds_read_b64_tr_b16 v[160:161], v0 offset:0x6c00
	ds_read_b64_tr_b16 v[162:163], v0 offset:0x7c00
	s_waitcnt lgkmcnt(0)
	v_mfma_f32_32x32x16_bf16 v[20:35], v[132:135], v[148:151], v[20:35]
	ds_read_b64_tr_b16 v[148:149], v0 offset:0xe00
	ds_read_b64_tr_b16 v[150:151], v0 offset:0x1e00
	v_mfma_f32_32x32x16_bf16 v[20:35], v[136:139], v[152:155], v[20:35]
	ds_read_b64_tr_b16 v[152:153], v0 offset:0x2e00
	ds_read_b64_tr_b16 v[154:155], v0 offset:0x3e00
	v_mfma_f32_32x32x16_bf16 v[20:35], v[140:143], v[156:159], v[20:35]
	ds_read_b64_tr_b16 v[156:157], v0 offset:0x4e00
	ds_read_b64_tr_b16 v[158:159], v0 offset:0x5e00
	v_mfma_f32_32x32x16_bf16 v[20:35], v[144:147], v[160:163], v[20:35]
	ds_read_b64_tr_b16 v[160:161], v0 offset:0x6e00
	ds_read_b64_tr_b16 v[162:163], v0 offset:0x7e00
	s_waitcnt lgkmcnt(0)
	v_mfma_f32_32x32x16_bf16 v[4:19], v[132:135], v[148:151], v[4:19]
	v_mfma_f32_32x32x16_bf16 v[4:19], v[136:139], v[152:155], v[4:19]
	v_mfma_f32_32x32x16_bf16 v[4:19], v[140:143], v[156:159], v[4:19]
	v_mfma_f32_32x32x16_bf16 v[4:19], v[144:147], v[160:163], v[4:19]
	v_mov_b32_e32 v132, v245
	s_nop 15
	s_branch .LBB0_946

; __global__ void __launch_bounds__(512, 2) fwd_kernel(Params p) {
	.amdhsa_kernel _Z10fwd_kernel6Params
		.amdhsa_group_segment_fixed_size 0
		.amdhsa_private_segment_fixed_size 0
		.amdhsa_kernarg_size 784
		.amdhsa_user_sgpr_count 2
		.amdhsa_user_sgpr_dispatch_ptr 0
		.amdhsa_user_sgpr_queue_ptr 0
		.amdhsa_user_sgpr_kernarg_segment_ptr 1
		.amdhsa_user_sgpr_dispatch_id 0
		.amdhsa_user_sgpr_kernarg_preload_length 0
		.amdhsa_user_sgpr_kernarg_preload_offset 0
		.amdhsa_user_sgpr_private_segment_size 0
		.amdhsa_uses_dynamic_stack 0
		.amdhsa_enable_private_segment 0
		.amdhsa_system_sgpr_workgroup_id_x 1
		.amdhsa_system_sgpr_workgroup_id_y 0
		.amdhsa_system_sgpr_workgroup_id_z 0
		.amdhsa_system_sgpr_workgroup_info 0
		.amdhsa_system_vgpr_workitem_id 0
		.amdhsa_next_free_vgpr 256
		.amdhsa_next_free_sgpr 102
		.amdhsa_accum_offset 256
		.amdhsa_reserve_vcc 1
		.amdhsa_float_round_mode_32 0
		.amdhsa_float_round_mode_16_64 0
		.amdhsa_float_denorm_mode_32 3
		.amdhsa_float_denorm_mode_16_64 3
		.amdhsa_dx10_clamp 1
		.amdhsa_ieee_mode 1
		.amdhsa_fp16_overflow 0
		.amdhsa_tg_split 0
		.amdhsa_exception_fp_ieee_invalid_op 0
		.amdhsa_exception_fp_denorm_src 0
		.amdhsa_exception_fp_ieee_div_zero 0
		.amdhsa_exception_fp_ieee_overflow 0
		.amdhsa_exception_fp_ieee_underflow 0
		.amdhsa_exception_fp_ieee_inexact 0
		.amdhsa_exception_int_div_zero 0
	.end_amdhsa_kernel

; __global__ void __launch_bounds__(512, 2) fwd_kernel(Params p) {
amdhsa.kernels:
  - .agpr_count:     0
    .args:
      - .offset:         0
        .size:           528
        .value_kind:     by_value
      - .offset:         528
        .size:           4
        .value_kind:     hidden_block_count_x
      - .offset:         532
        .size:           4
        .value_kind:     hidden_block_count_y
      - .offset:         536
        .size:           4
        .value_kind:     hidden_block_count_z
      - .offset:         540
        .size:           2
        .value_kind:     hidden_group_size_x
      - .offset:         542
        .size:           2
        .value_kind:     hidden_group_size_y
      - .offset:         544
        .size:           2
        .value_kind:     hidden_group_size_z
      - .offset:         546
        .size:           2
        .value_kind:     hidden_remainder_x
      - .offset:         548
        .size:           2
        .value_kind:     hidden_remainder_y
      - .offset:         550
        .size:           2
        .value_kind:     hidden_remainder_z
      - .offset:         568
        .size:           8
        .value_kind:     hidden_global_offset_x
      - .offset:         576
        .size:           8
        .value_kind:     hidden_global_offset_y
      - .offset:         584
        .size:           8
        .value_kind:     hidden_global_offset_z
      - .offset:         592
        .size:           2
        .value_kind:     hidden_grid_dims
      - .offset:         648
        .size:           4
        .value_kind:     hidden_dynamic_lds_size
    .group_segment_fixed_size: 0
    .kernarg_segment_align: 8
    .kernarg_segment_size: 784
    .language:       OpenCL C
    .language_version:
      - 2
      - 0
    .max_flat_workgroup_size: 512
    .name:           _Z10fwd_kernel6Params
    .private_segment_fixed_size: 0
    .sgpr_count:     108
    .sgpr_spill_count: 12
    .symbol:         _Z10fwd_kernel6Params.kd
    .uniform_work_group_size: 1
    .uses_dynamic_stack: false
    .vgpr_count:     256
    .vgpr_spill_count: 0
    .wavefront_size: 64
